# scan: v operand pair fetched with one ds_read_b64 from a pair-duplicated LDS image, dead last-step reads dropped
# baseline (speedup 1.0000x reference)
; #define LAS __attribute__((address_space(3)))
; #define P4_RDSET(P, base_, boff_, vo_, vt_, voff_) do { P##w = lds_rd128<(boff_)>(base_); P##a = lds_rd128<(boff_) + SB * 256>(base_); P##b = lds_rd128<(boff_) + 2 * SB * 256>(base_); \
;                     P##k = lds_rd128<(boff_) + 3 * SB * 256>(base_); P##r = lds_rd128<(boff_) + 4 * SB * 256>(base_); P##vo = lds_rd32<(voff_)>(vo_); P##vt = lds_rd32<(voff_)>(vt_); } while (0)
; __device__ __forceinline__ void p4_scan(Frame& F) {
;     ...
;             for (int blk = 0; blk < NBLK; ++blk) {
;                 const LAS unsigned char* sb = F.lds + (blk & 1) * SLOT_BYTES;
;                 LAS float* yb = (LAS float*)(F.lds + YB_OFF + (blk & 1) * YB_BYTES);
;                 const unsigned aK = (unsigned)(size_t)(sb) + kap * 16, aVo = (unsigned)(size_t)(sb) + 5 * (SB * 256) + rown * 4, aVt = (unsigned)(size_t)(sb) + 5 * (SB * 256) + roth * 4;
;                 f32x4 cw, ca, cb, ck, cr; float cvo, cvt;
;     ...
;                 P4_RDSET(c, aK, 0, aVo, aVt, 0);
;                 asm volatile("s_waitcnt lgkmcnt(0)" : P4_TIE(c));
;                 {
;                     float ykeep = 0.f; const unsigned aK0 = aK, aVo0 = aVo, aVt0 = aVt;
.LBB0_489:
	s_and_b32 s3, s2, 1
	s_mul_i32 s22, s3, 0xb000
	v_lshl_add_u32 v78, s3, 12, v155
	v_lshl_add_u32 v197, s3, 12, v196
	v_mov_b32_e32 v198, 0x20400
	v_lshl_add_u32 v198, s3, 13, v198
	v_lshl_add_u32 v198, v99, 1, v198
	s_add_i32 s3, s22, 0
	v_add_u32_e32 v79, s3, v91
	s_add_i32 s3, s3, 0xa000
	v_add_u32_e32 v80, s3, v99
	v_add_u32_e32 v81, s3, v103
	ds_read_b128 v[82:85], v79 offset:0
	ds_read_b128 v[86:89], v79 offset:0x2000
	ds_read_b128 v[114:117], v79 offset:0x4000
	ds_read_b128 v[118:121], v79 offset:0x6000
	ds_read_b128 v[122:125], v79 offset:0x8000
	ds_read_b64 v[126:127], v198 offset:0
	s_add_i32 s2, s2, 1
	s_waitcnt lgkmcnt(0)
	ds_read_b128 v[162:165], v79 offset:0x100
	ds_read_b128 v[166:169], v79 offset:0x2100
	ds_read_b128 v[170:173], v79 offset:0x4100
	ds_read_b128 v[174:177], v79 offset:0x6100
	ds_read_b128 v[178:181], v79 offset:0x8100
	ds_read_b64 v[182:183], v198 offset:256
	v_pk_mul_f32 v[250:251], v[70:71], v[86:87] op_sel_hi:[1,0]
	v_pk_fma_f32 v[250:251], v[72:73], v[86:87], v[250:251] op_sel:[0,1,0] op_sel_hi:[1,1,1]
	v_pk_fma_f32 v[250:251], v[74:75], v[88:89], v[250:251] op_sel_hi:[1,0,1]
	v_pk_fma_f32 v[250:251], v[76:77], v[88:89], v[250:251] op_sel:[0,1,0] op_sel_hi:[1,1,1]
	v_pk_mul_f32 v[184:185], v[126:127], v[118:119] op_sel_hi:[1,0]
	v_pk_mul_f32 v[186:187], v[126:127], v[118:119] op_sel:[0,1] op_sel_hi:[1,1]
	v_add_f32_dpp v252, v251, v250 quad_perm:[1,0,3,2] row_mask:0xf bank_mask:0xf bound_ctrl:1
	s_nop 0
	v_pk_mul_f32 v[188:189], v[126:127], v[120:121] op_sel_hi:[1,0]
	v_add_f32_dpp v252, v252, v252 quad_perm:[2,3,0,1] row_mask:0xf bank_mask:0xf bound_ctrl:1
	s_nop 0
	v_pk_mul_f32 v[190:191], v[126:127], v[120:121] op_sel:[0,1] op_sel_hi:[1,1]
	v_add_f32_dpp v252, v252, v252 row_ror:4 row_mask:0xf bank_mask:0xf bound_ctrl:1
	s_nop 0
	v_pk_fma_f32 v[184:185], v[70:71], v[82:83], v[184:185] op_sel_hi:[1,0,1]
	v_add_f32_dpp v252, v252, v252 row_ror:8 row_mask:0xf bank_mask:0xf bound_ctrl:1
	s_nop 0
	v_pk_fma_f32 v[186:187], v[72:73], v[82:83], v[186:187] op_sel:[0,1,0] op_sel_hi:[1,1,1]
	v_mov_b32_dpp v253, v252 quad_perm:[1,0,3,2] row_mask:0xf bank_mask:0xf bound_ctrl:1
	v_pk_fma_f32 v[188:189], v[74:75], v[84:85], v[188:189] op_sel_hi:[1,0,1]
	v_pk_fma_f32 v[190:191], v[76:77], v[84:85], v[190:191] op_sel:[0,1,0] op_sel_hi:[1,1,1]
	v_pk_fma_f32 v[70:71], v[252:253], v[114:115], v[184:185] op_sel_hi:[1,0,1]
	v_pk_fma_f32 v[72:73], v[252:253], v[114:115], v[186:187] op_sel:[0,1,0] op_sel_hi:[1,1,1]
	v_pk_fma_f32 v[74:75], v[252:253], v[116:117], v[188:189] op_sel_hi:[1,0,1]
	v_pk_fma_f32 v[76:77], v[252:253], v[116:117], v[190:191] op_sel:[0,1,0] op_sel_hi:[1,1,1]
	v_pk_mul_f32 v[192:193], v[70:71], v[122:123] op_sel_hi:[1,0]
	v_pk_fma_f32 v[192:193], v[72:73], v[122:123], v[192:193] op_sel:[0,1,0] op_sel_hi:[1,1,1]
	v_pk_fma_f32 v[192:193], v[74:75], v[124:125], v[192:193] op_sel_hi:[1,0,1]
	v_pk_fma_f32 v[192:193], v[76:77], v[124:125], v[192:193] op_sel:[0,1,0] op_sel_hi:[1,1,1]

	s_cmpk_lg_i32 s2, 0x88
	s_waitcnt lgkmcnt(0)
	s_nop 0
	ds_read_b128 v[82:85], v79 offset:0x200
	ds_read_b128 v[86:89], v79 offset:0x2200
	ds_read_b128 v[114:117], v79 offset:0x4200
	ds_read_b128 v[118:121], v79 offset:0x6200
	ds_read_b128 v[122:125], v79 offset:0x8200
	ds_read_b64 v[126:127], v198 offset:512
	v_pk_mul_f32 v[250:251], v[70:71], v[166:167] op_sel_hi:[1,0]
	v_pk_fma_f32 v[250:251], v[72:73], v[166:167], v[250:251] op_sel:[0,1,0] op_sel_hi:[1,1,1]
	v_pk_fma_f32 v[250:251], v[74:75], v[168:169], v[250:251] op_sel_hi:[1,0,1]
	v_pk_fma_f32 v[250:251], v[76:77], v[168:169], v[250:251] op_sel:[0,1,0] op_sel_hi:[1,1,1]
	v_pk_mul_f32 v[184:185], v[182:183], v[174:175] op_sel_hi:[1,0]
	v_pk_mul_f32 v[186:187], v[182:183], v[174:175] op_sel:[0,1] op_sel_hi:[1,1]
	v_add_f32_dpp v252, v251, v250 quad_perm:[1,0,3,2] row_mask:0xf bank_mask:0xf bound_ctrl:1
	v_add_f32_dpp v92, v193, v192 quad_perm:[1,0,3,2] row_mask:0xf bank_mask:0xf bound_ctrl:1
	v_pk_mul_f32 v[188:189], v[182:183], v[176:177] op_sel_hi:[1,0]
	v_add_f32_dpp v252, v252, v252 quad_perm:[2,3,0,1] row_mask:0xf bank_mask:0xf bound_ctrl:1
	v_add_f32_dpp v92, v92, v92 quad_perm:[2,3,0,1] row_mask:0xf bank_mask:0xf bound_ctrl:1
	v_pk_mul_f32 v[190:191], v[182:183], v[176:177] op_sel:[0,1] op_sel_hi:[1,1]
	v_add_f32_dpp v252, v252, v252 row_ror:4 row_mask:0xf bank_mask:0xf bound_ctrl:1
	v_add_f32_dpp v92, v92, v92 row_ror:4 row_mask:0xf bank_mask:0xf bound_ctrl:1
	v_pk_fma_f32 v[184:185], v[70:71], v[162:163], v[184:185] op_sel_hi:[1,0,1]
	v_add_f32_dpp v252, v252, v252 row_ror:8 row_mask:0xf bank_mask:0xf bound_ctrl:1
	v_add_f32_dpp v92, v92, v92 row_ror:8 row_mask:0xf bank_mask:0x1 bound_ctrl:1
	v_pk_fma_f32 v[186:187], v[72:73], v[162:163], v[186:187] op_sel:[0,1,0] op_sel_hi:[1,1,1]
	v_mov_b32_dpp v253, v252 quad_perm:[1,0,3,2] row_mask:0xf bank_mask:0xf bound_ctrl:1
	v_pk_fma_f32 v[188:189], v[74:75], v[164:165], v[188:189] op_sel_hi:[1,0,1]
	v_pk_fma_f32 v[190:191], v[76:77], v[164:165], v[190:191] op_sel:[0,1,0] op_sel_hi:[1,1,1]
	v_pk_fma_f32 v[70:71], v[252:253], v[170:171], v[184:185] op_sel_hi:[1,0,1]
	v_pk_fma_f32 v[72:73], v[252:253], v[170:171], v[186:187] op_sel:[0,1,0] op_sel_hi:[1,1,1]
	v_pk_fma_f32 v[74:75], v[252:253], v[172:173], v[188:189] op_sel_hi:[1,0,1]
	v_pk_fma_f32 v[76:77], v[252:253], v[172:173], v[190:191] op_sel:[0,1,0] op_sel_hi:[1,1,1]
	v_pk_mul_f32 v[194:195], v[70:71], v[178:179] op_sel_hi:[1,0]
	v_pk_fma_f32 v[194:195], v[72:73], v[178:179], v[194:195] op_sel:[0,1,0] op_sel_hi:[1,1,1]
	v_pk_fma_f32 v[194:195], v[74:75], v[180:181], v[194:195] op_sel_hi:[1,0,1]
	v_pk_fma_f32 v[194:195], v[76:77], v[180:181], v[194:195] op_sel:[0,1,0] op_sel_hi:[1,1,1]

	s_waitcnt lgkmcnt(0)
	ds_read_b128 v[162:165], v79 offset:0x300
	ds_read_b128 v[166:169], v79 offset:0x2300
	ds_read_b128 v[170:173], v79 offset:0x4300
	ds_read_b128 v[174:177], v79 offset:0x6300
	ds_read_b128 v[178:181], v79 offset:0x8300
	ds_read_b64 v[182:183], v198 offset:768
	v_pk_mul_f32 v[250:251], v[70:71], v[86:87] op_sel_hi:[1,0]
	v_pk_fma_f32 v[250:251], v[72:73], v[86:87], v[250:251] op_sel:[0,1,0] op_sel_hi:[1,1,1]
	v_pk_fma_f32 v[250:251], v[74:75], v[88:89], v[250:251] op_sel_hi:[1,0,1]
	v_pk_fma_f32 v[250:251], v[76:77], v[88:89], v[250:251] op_sel:[0,1,0] op_sel_hi:[1,1,1]
	v_pk_mul_f32 v[184:185], v[126:127], v[118:119] op_sel_hi:[1,0]
	v_pk_mul_f32 v[186:187], v[126:127], v[118:119] op_sel:[0,1] op_sel_hi:[1,1]
	v_add_f32_dpp v252, v251, v250 quad_perm:[1,0,3,2] row_mask:0xf bank_mask:0xf bound_ctrl:1
	v_add_f32_dpp v161, v195, v194 quad_perm:[1,0,3,2] row_mask:0xf bank_mask:0xf bound_ctrl:1
	v_pk_mul_f32 v[188:189], v[126:127], v[120:121] op_sel_hi:[1,0]
	v_add_f32_dpp v252, v252, v252 quad_perm:[2,3,0,1] row_mask:0xf bank_mask:0xf bound_ctrl:1
	v_add_f32_dpp v161, v161, v161 quad_perm:[2,3,0,1] row_mask:0xf bank_mask:0xf bound_ctrl:1
	v_pk_mul_f32 v[190:191], v[126:127], v[120:121] op_sel:[0,1] op_sel_hi:[1,1]
	v_add_f32_dpp v252, v252, v252 row_ror:4 row_mask:0xf bank_mask:0xf bound_ctrl:1
	v_add_f32_dpp v161, v161, v161 row_ror:4 row_mask:0xf bank_mask:0xf bound_ctrl:1
	v_pk_fma_f32 v[184:185], v[70:71], v[82:83], v[184:185] op_sel_hi:[1,0,1]
	v_add_f32_dpp v252, v252, v252 row_ror:8 row_mask:0xf bank_mask:0xf bound_ctrl:1
	v_add_f32_dpp v92, v161, v161 row_ror:8 row_mask:0xf bank_mask:0x2 bound_ctrl:1
	v_pk_fma_f32 v[186:187], v[72:73], v[82:83], v[186:187] op_sel:[0,1,0] op_sel_hi:[1,1,1]
	v_mov_b32_dpp v253, v252 quad_perm:[1,0,3,2] row_mask:0xf bank_mask:0xf bound_ctrl:1
	v_pk_fma_f32 v[188:189], v[74:75], v[84:85], v[188:189] op_sel_hi:[1,0,1]
	v_pk_fma_f32 v[190:191], v[76:77], v[84:85], v[190:191] op_sel:[0,1,0] op_sel_hi:[1,1,1]
	v_pk_fma_f32 v[70:71], v[252:253], v[114:115], v[184:185] op_sel_hi:[1,0,1]
	v_pk_fma_f32 v[72:73], v[252:253], v[114:115], v[186:187] op_sel:[0,1,0] op_sel_hi:[1,1,1]
	v_pk_fma_f32 v[74:75], v[252:253], v[116:117], v[188:189] op_sel_hi:[1,0,1]
	v_pk_fma_f32 v[76:77], v[252:253], v[116:117], v[190:191] op_sel:[0,1,0] op_sel_hi:[1,1,1]
	v_pk_mul_f32 v[192:193], v[70:71], v[122:123] op_sel_hi:[1,0]
	v_pk_fma_f32 v[192:193], v[72:73], v[122:123], v[192:193] op_sel:[0,1,0] op_sel_hi:[1,1,1]
	v_pk_fma_f32 v[192:193], v[74:75], v[124:125], v[192:193] op_sel_hi:[1,0,1]
	v_pk_fma_f32 v[192:193], v[76:77], v[124:125], v[192:193] op_sel:[0,1,0] op_sel_hi:[1,1,1]

	s_waitcnt lgkmcnt(0)
	ds_read_b128 v[82:85], v79 offset:0x400
	ds_read_b128 v[86:89], v79 offset:0x2400
	ds_read_b128 v[114:117], v79 offset:0x4400
	ds_read_b128 v[118:121], v79 offset:0x6400
	ds_read_b128 v[122:125], v79 offset:0x8400
	ds_read_b64 v[126:127], v198 offset:1024
	v_pk_mul_f32 v[250:251], v[70:71], v[166:167] op_sel_hi:[1,0]
	v_pk_fma_f32 v[250:251], v[72:73], v[166:167], v[250:251] op_sel:[0,1,0] op_sel_hi:[1,1,1]
	v_pk_fma_f32 v[250:251], v[74:75], v[168:169], v[250:251] op_sel_hi:[1,0,1]
	v_pk_fma_f32 v[250:251], v[76:77], v[168:169], v[250:251] op_sel:[0,1,0] op_sel_hi:[1,1,1]
	v_pk_mul_f32 v[184:185], v[182:183], v[174:175] op_sel_hi:[1,0]
	v_pk_mul_f32 v[186:187], v[182:183], v[174:175] op_sel:[0,1] op_sel_hi:[1,1]
	v_add_f32_dpp v252, v251, v250 quad_perm:[1,0,3,2] row_mask:0xf bank_mask:0xf bound_ctrl:1
	v_add_f32_dpp v161, v193, v192 quad_perm:[1,0,3,2] row_mask:0xf bank_mask:0xf bound_ctrl:1
	v_pk_mul_f32 v[188:189], v[182:183], v[176:177] op_sel_hi:[1,0]
	v_add_f32_dpp v252, v252, v252 quad_perm:[2,3,0,1] row_mask:0xf bank_mask:0xf bound_ctrl:1
	v_add_f32_dpp v161, v161, v161 quad_perm:[2,3,0,1] row_mask:0xf bank_mask:0xf bound_ctrl:1
	v_pk_mul_f32 v[190:191], v[182:183], v[176:177] op_sel:[0,1] op_sel_hi:[1,1]
	v_add_f32_dpp v252, v252, v252 row_ror:4 row_mask:0xf bank_mask:0xf bound_ctrl:1
	v_add_f32_dpp v161, v161, v161 row_ror:4 row_mask:0xf bank_mask:0xf bound_ctrl:1
	v_pk_fma_f32 v[184:185], v[70:71], v[162:163], v[184:185] op_sel_hi:[1,0,1]
	v_add_f32_dpp v252, v252, v252 row_ror:8 row_mask:0xf bank_mask:0xf bound_ctrl:1
	v_add_f32_dpp v92, v161, v161 row_ror:8 row_mask:0xf bank_mask:0x4 bound_ctrl:1
	v_pk_fma_f32 v[186:187], v[72:73], v[162:163], v[186:187] op_sel:[0,1,0] op_sel_hi:[1,1,1]
	v_mov_b32_dpp v253, v252 quad_perm:[1,0,3,2] row_mask:0xf bank_mask:0xf bound_ctrl:1
	v_pk_fma_f32 v[188:189], v[74:75], v[164:165], v[188:189] op_sel_hi:[1,0,1]
	v_pk_fma_f32 v[190:191], v[76:77], v[164:165], v[190:191] op_sel:[0,1,0] op_sel_hi:[1,1,1]
	v_pk_fma_f32 v[70:71], v[252:253], v[170:171], v[184:185] op_sel_hi:[1,0,1]
	v_pk_fma_f32 v[72:73], v[252:253], v[170:171], v[186:187] op_sel:[0,1,0] op_sel_hi:[1,1,1]
	v_pk_fma_f32 v[74:75], v[252:253], v[172:173], v[188:189] op_sel_hi:[1,0,1]
	v_pk_fma_f32 v[76:77], v[252:253], v[172:173], v[190:191] op_sel:[0,1,0] op_sel_hi:[1,1,1]
	v_pk_mul_f32 v[194:195], v[70:71], v[178:179] op_sel_hi:[1,0]
	v_pk_fma_f32 v[194:195], v[72:73], v[178:179], v[194:195] op_sel:[0,1,0] op_sel_hi:[1,1,1]
	v_pk_fma_f32 v[194:195], v[74:75], v[180:181], v[194:195] op_sel_hi:[1,0,1]
	v_pk_fma_f32 v[194:195], v[76:77], v[180:181], v[194:195] op_sel:[0,1,0] op_sel_hi:[1,1,1]

	s_waitcnt lgkmcnt(0)
	ds_read_b128 v[162:165], v79 offset:0x500
	ds_read_b128 v[166:169], v79 offset:0x2500
	ds_read_b128 v[170:173], v79 offset:0x4500
	ds_read_b128 v[174:177], v79 offset:0x6500
	ds_read_b128 v[178:181], v79 offset:0x8500
	ds_read_b64 v[182:183], v198 offset:1280
	v_pk_mul_f32 v[250:251], v[70:71], v[86:87] op_sel_hi:[1,0]
	v_pk_fma_f32 v[250:251], v[72:73], v[86:87], v[250:251] op_sel:[0,1,0] op_sel_hi:[1,1,1]
	v_pk_fma_f32 v[250:251], v[74:75], v[88:89], v[250:251] op_sel_hi:[1,0,1]
	v_pk_fma_f32 v[250:251], v[76:77], v[88:89], v[250:251] op_sel:[0,1,0] op_sel_hi:[1,1,1]
	v_pk_mul_f32 v[184:185], v[126:127], v[118:119] op_sel_hi:[1,0]
	v_pk_mul_f32 v[186:187], v[126:127], v[118:119] op_sel:[0,1] op_sel_hi:[1,1]
	v_add_f32_dpp v252, v251, v250 quad_perm:[1,0,3,2] row_mask:0xf bank_mask:0xf bound_ctrl:1
	v_add_f32_dpp v161, v195, v194 quad_perm:[1,0,3,2] row_mask:0xf bank_mask:0xf bound_ctrl:1
	v_pk_mul_f32 v[188:189], v[126:127], v[120:121] op_sel_hi:[1,0]
	v_add_f32_dpp v252, v252, v252 quad_perm:[2,3,0,1] row_mask:0xf bank_mask:0xf bound_ctrl:1
	v_add_f32_dpp v161, v161, v161 quad_perm:[2,3,0,1] row_mask:0xf bank_mask:0xf bound_ctrl:1
	v_pk_mul_f32 v[190:191], v[126:127], v[120:121] op_sel:[0,1] op_sel_hi:[1,1]
	v_add_f32_dpp v252, v252, v252 row_ror:4 row_mask:0xf bank_mask:0xf bound_ctrl:1
	v_add_f32_dpp v161, v161, v161 row_ror:4 row_mask:0xf bank_mask:0xf bound_ctrl:1
	v_pk_fma_f32 v[184:185], v[70:71], v[82:83], v[184:185] op_sel_hi:[1,0,1]
	v_add_f32_dpp v252, v252, v252 row_ror:8 row_mask:0xf bank_mask:0xf bound_ctrl:1
	v_add_f32_dpp v92, v161, v161 row_ror:8 row_mask:0xf bank_mask:0x8 bound_ctrl:1
	v_pk_fma_f32 v[186:187], v[72:73], v[82:83], v[186:187] op_sel:[0,1,0] op_sel_hi:[1,1,1]
	v_mov_b32_dpp v253, v252 quad_perm:[1,0,3,2] row_mask:0xf bank_mask:0xf bound_ctrl:1
	v_pk_fma_f32 v[188:189], v[74:75], v[84:85], v[188:189] op_sel_hi:[1,0,1]
	v_pk_fma_f32 v[190:191], v[76:77], v[84:85], v[190:191] op_sel:[0,1,0] op_sel_hi:[1,1,1]
	v_pk_fma_f32 v[70:71], v[252:253], v[114:115], v[184:185] op_sel_hi:[1,0,1]
	v_pk_fma_f32 v[72:73], v[252:253], v[114:115], v[186:187] op_sel:[0,1,0] op_sel_hi:[1,1,1]
	v_pk_fma_f32 v[74:75], v[252:253], v[116:117], v[188:189] op_sel_hi:[1,0,1]
	v_pk_fma_f32 v[76:77], v[252:253], v[116:117], v[190:191] op_sel:[0,1,0] op_sel_hi:[1,1,1]
	v_pk_mul_f32 v[192:193], v[70:71], v[122:123] op_sel_hi:[1,0]
	v_pk_fma_f32 v[192:193], v[72:73], v[122:123], v[192:193] op_sel:[0,1,0] op_sel_hi:[1,1,1]
	v_pk_fma_f32 v[192:193], v[74:75], v[124:125], v[192:193] op_sel_hi:[1,0,1]
	v_pk_fma_f32 v[192:193], v[76:77], v[124:125], v[192:193] op_sel:[0,1,0] op_sel_hi:[1,1,1]

	s_waitcnt lgkmcnt(0)
	ds_write_b32 v197, v92 offset:0
	ds_read_b128 v[82:85], v79 offset:0x600
	ds_read_b128 v[86:89], v79 offset:0x2600
	ds_read_b128 v[114:117], v79 offset:0x4600
	ds_read_b128 v[118:121], v79 offset:0x6600
	ds_read_b128 v[122:125], v79 offset:0x8600
	ds_read_b64 v[126:127], v198 offset:1536
	v_pk_mul_f32 v[250:251], v[70:71], v[166:167] op_sel_hi:[1,0]
	v_pk_fma_f32 v[250:251], v[72:73], v[166:167], v[250:251] op_sel:[0,1,0] op_sel_hi:[1,1,1]
	v_pk_fma_f32 v[250:251], v[74:75], v[168:169], v[250:251] op_sel_hi:[1,0,1]
	v_pk_fma_f32 v[250:251], v[76:77], v[168:169], v[250:251] op_sel:[0,1,0] op_sel_hi:[1,1,1]
	v_pk_mul_f32 v[184:185], v[182:183], v[174:175] op_sel_hi:[1,0]
	v_pk_mul_f32 v[186:187], v[182:183], v[174:175] op_sel:[0,1] op_sel_hi:[1,1]
	v_add_f32_dpp v252, v251, v250 quad_perm:[1,0,3,2] row_mask:0xf bank_mask:0xf bound_ctrl:1
	v_add_f32_dpp v161, v193, v192 quad_perm:[1,0,3,2] row_mask:0xf bank_mask:0xf bound_ctrl:1
	v_pk_mul_f32 v[188:189], v[182:183], v[176:177] op_sel_hi:[1,0]
	v_add_f32_dpp v252, v252, v252 quad_perm:[2,3,0,1] row_mask:0xf bank_mask:0xf bound_ctrl:1
	v_add_f32_dpp v161, v161, v161 quad_perm:[2,3,0,1] row_mask:0xf bank_mask:0xf bound_ctrl:1
	v_pk_mul_f32 v[190:191], v[182:183], v[176:177] op_sel:[0,1] op_sel_hi:[1,1]
	v_add_f32_dpp v252, v252, v252 row_ror:4 row_mask:0xf bank_mask:0xf bound_ctrl:1
	v_add_f32_dpp v161, v161, v161 row_ror:4 row_mask:0xf bank_mask:0xf bound_ctrl:1
	v_pk_fma_f32 v[184:185], v[70:71], v[162:163], v[184:185] op_sel_hi:[1,0,1]
	v_add_f32_dpp v252, v252, v252 row_ror:8 row_mask:0xf bank_mask:0xf bound_ctrl:1
	v_add_f32_dpp v92, v161, v161 row_ror:8 row_mask:0xf bank_mask:0x1 bound_ctrl:1
	v_pk_fma_f32 v[186:187], v[72:73], v[162:163], v[186:187] op_sel:[0,1,0] op_sel_hi:[1,1,1]
	v_mov_b32_dpp v253, v252 quad_perm:[1,0,3,2] row_mask:0xf bank_mask:0xf bound_ctrl:1
	v_pk_fma_f32 v[188:189], v[74:75], v[164:165], v[188:189] op_sel_hi:[1,0,1]
	v_pk_fma_f32 v[190:191], v[76:77], v[164:165], v[190:191] op_sel:[0,1,0] op_sel_hi:[1,1,1]
	v_pk_fma_f32 v[70:71], v[252:253], v[170:171], v[184:185] op_sel_hi:[1,0,1]
	v_pk_fma_f32 v[72:73], v[252:253], v[170:171], v[186:187] op_sel:[0,1,0] op_sel_hi:[1,1,1]
	v_pk_fma_f32 v[74:75], v[252:253], v[172:173], v[188:189] op_sel_hi:[1,0,1]
	v_pk_fma_f32 v[76:77], v[252:253], v[172:173], v[190:191] op_sel:[0,1,0] op_sel_hi:[1,1,1]
	v_pk_mul_f32 v[194:195], v[70:71], v[178:179] op_sel_hi:[1,0]
	v_pk_fma_f32 v[194:195], v[72:73], v[178:179], v[194:195] op_sel:[0,1,0] op_sel_hi:[1,1,1]
	v_pk_fma_f32 v[194:195], v[74:75], v[180:181], v[194:195] op_sel_hi:[1,0,1]
	v_pk_fma_f32 v[194:195], v[76:77], v[180:181], v[194:195] op_sel:[0,1,0] op_sel_hi:[1,1,1]

	s_waitcnt lgkmcnt(0)
	ds_read_b128 v[162:165], v79 offset:0x700
	ds_read_b128 v[166:169], v79 offset:0x2700
	ds_read_b128 v[170:173], v79 offset:0x4700
	ds_read_b128 v[174:177], v79 offset:0x6700
	ds_read_b128 v[178:181], v79 offset:0x8700
	ds_read_b64 v[182:183], v198 offset:1792
	v_pk_mul_f32 v[250:251], v[70:71], v[86:87] op_sel_hi:[1,0]
	v_pk_fma_f32 v[250:251], v[72:73], v[86:87], v[250:251] op_sel:[0,1,0] op_sel_hi:[1,1,1]
	v_pk_fma_f32 v[250:251], v[74:75], v[88:89], v[250:251] op_sel_hi:[1,0,1]
	v_pk_fma_f32 v[250:251], v[76:77], v[88:89], v[250:251] op_sel:[0,1,0] op_sel_hi:[1,1,1]
	v_pk_mul_f32 v[184:185], v[126:127], v[118:119] op_sel_hi:[1,0]
	v_pk_mul_f32 v[186:187], v[126:127], v[118:119] op_sel:[0,1] op_sel_hi:[1,1]
	v_add_f32_dpp v252, v251, v250 quad_perm:[1,0,3,2] row_mask:0xf bank_mask:0xf bound_ctrl:1
	v_add_f32_dpp v161, v195, v194 quad_perm:[1,0,3,2] row_mask:0xf bank_mask:0xf bound_ctrl:1
	v_pk_mul_f32 v[188:189], v[126:127], v[120:121] op_sel_hi:[1,0]
	v_add_f32_dpp v252, v252, v252 quad_perm:[2,3,0,1] row_mask:0xf bank_mask:0xf bound_ctrl:1
	v_add_f32_dpp v161, v161, v161 quad_perm:[2,3,0,1] row_mask:0xf bank_mask:0xf bound_ctrl:1
	v_pk_mul_f32 v[190:191], v[126:127], v[120:121] op_sel:[0,1] op_sel_hi:[1,1]
	v_add_f32_dpp v252, v252, v252 row_ror:4 row_mask:0xf bank_mask:0xf bound_ctrl:1
	v_add_f32_dpp v161, v161, v161 row_ror:4 row_mask:0xf bank_mask:0xf bound_ctrl:1
	v_pk_fma_f32 v[184:185], v[70:71], v[82:83], v[184:185] op_sel_hi:[1,0,1]
	v_add_f32_dpp v252, v252, v252 row_ror:8 row_mask:0xf bank_mask:0xf bound_ctrl:1
	v_add_f32_dpp v92, v161, v161 row_ror:8 row_mask:0xf bank_mask:0x2 bound_ctrl:1
	v_pk_fma_f32 v[186:187], v[72:73], v[82:83], v[186:187] op_sel:[0,1,0] op_sel_hi:[1,1,1]
	v_mov_b32_dpp v253, v252 quad_perm:[1,0,3,2] row_mask:0xf bank_mask:0xf bound_ctrl:1
	v_pk_fma_f32 v[188:189], v[74:75], v[84:85], v[188:189] op_sel_hi:[1,0,1]
	v_pk_fma_f32 v[190:191], v[76:77], v[84:85], v[190:191] op_sel:[0,1,0] op_sel_hi:[1,1,1]
	v_pk_fma_f32 v[70:71], v[252:253], v[114:115], v[184:185] op_sel_hi:[1,0,1]
	v_pk_fma_f32 v[72:73], v[252:253], v[114:115], v[186:187] op_sel:[0,1,0] op_sel_hi:[1,1,1]
	v_pk_fma_f32 v[74:75], v[252:253], v[116:117], v[188:189] op_sel_hi:[1,0,1]
	v_pk_fma_f32 v[76:77], v[252:253], v[116:117], v[190:191] op_sel:[0,1,0] op_sel_hi:[1,1,1]
	v_pk_mul_f32 v[192:193], v[70:71], v[122:123] op_sel_hi:[1,0]
	v_pk_fma_f32 v[192:193], v[72:73], v[122:123], v[192:193] op_sel:[0,1,0] op_sel_hi:[1,1,1]
	v_pk_fma_f32 v[192:193], v[74:75], v[124:125], v[192:193] op_sel_hi:[1,0,1]
	v_pk_fma_f32 v[192:193], v[76:77], v[124:125], v[192:193] op_sel:[0,1,0] op_sel_hi:[1,1,1]

	s_waitcnt lgkmcnt(0)
	ds_read_b128 v[82:85], v79 offset:0x800
	ds_read_b128 v[86:89], v79 offset:0x2800
	ds_read_b128 v[114:117], v79 offset:0x4800
	ds_read_b128 v[118:121], v79 offset:0x6800
	ds_read_b128 v[122:125], v79 offset:0x8800
	ds_read_b64 v[126:127], v198 offset:2048
	v_pk_mul_f32 v[250:251], v[70:71], v[166:167] op_sel_hi:[1,0]
	v_pk_fma_f32 v[250:251], v[72:73], v[166:167], v[250:251] op_sel:[0,1,0] op_sel_hi:[1,1,1]
	v_pk_fma_f32 v[250:251], v[74:75], v[168:169], v[250:251] op_sel_hi:[1,0,1]
	v_pk_fma_f32 v[250:251], v[76:77], v[168:169], v[250:251] op_sel:[0,1,0] op_sel_hi:[1,1,1]
	v_pk_mul_f32 v[184:185], v[182:183], v[174:175] op_sel_hi:[1,0]
	v_pk_mul_f32 v[186:187], v[182:183], v[174:175] op_sel:[0,1] op_sel_hi:[1,1]
	v_add_f32_dpp v252, v251, v250 quad_perm:[1,0,3,2] row_mask:0xf bank_mask:0xf bound_ctrl:1
	v_add_f32_dpp v161, v193, v192 quad_perm:[1,0,3,2] row_mask:0xf bank_mask:0xf bound_ctrl:1
	v_pk_mul_f32 v[188:189], v[182:183], v[176:177] op_sel_hi:[1,0]
	v_add_f32_dpp v252, v252, v252 quad_perm:[2,3,0,1] row_mask:0xf bank_mask:0xf bound_ctrl:1
	v_add_f32_dpp v161, v161, v161 quad_perm:[2,3,0,1] row_mask:0xf bank_mask:0xf bound_ctrl:1
	v_pk_mul_f32 v[190:191], v[182:183], v[176:177] op_sel:[0,1] op_sel_hi:[1,1]
	v_add_f32_dpp v252, v252, v252 row_ror:4 row_mask:0xf bank_mask:0xf bound_ctrl:1
	v_add_f32_dpp v161, v161, v161 row_ror:4 row_mask:0xf bank_mask:0xf bound_ctrl:1
	v_pk_fma_f32 v[184:185], v[70:71], v[162:163], v[184:185] op_sel_hi:[1,0,1]
	v_add_f32_dpp v252, v252, v252 row_ror:8 row_mask:0xf bank_mask:0xf bound_ctrl:1
	v_add_f32_dpp v92, v161, v161 row_ror:8 row_mask:0xf bank_mask:0x4 bound_ctrl:1
	v_pk_fma_f32 v[186:187], v[72:73], v[162:163], v[186:187] op_sel:[0,1,0] op_sel_hi:[1,1,1]
	v_mov_b32_dpp v253, v252 quad_perm:[1,0,3,2] row_mask:0xf bank_mask:0xf bound_ctrl:1
	v_pk_fma_f32 v[188:189], v[74:75], v[164:165], v[188:189] op_sel_hi:[1,0,1]
	v_pk_fma_f32 v[190:191], v[76:77], v[164:165], v[190:191] op_sel:[0,1,0] op_sel_hi:[1,1,1]
	v_pk_fma_f32 v[70:71], v[252:253], v[170:171], v[184:185] op_sel_hi:[1,0,1]
	v_pk_fma_f32 v[72:73], v[252:253], v[170:171], v[186:187] op_sel:[0,1,0] op_sel_hi:[1,1,1]
	v_pk_fma_f32 v[74:75], v[252:253], v[172:173], v[188:189] op_sel_hi:[1,0,1]
	v_pk_fma_f32 v[76:77], v[252:253], v[172:173], v[190:191] op_sel:[0,1,0] op_sel_hi:[1,1,1]
	v_pk_mul_f32 v[194:195], v[70:71], v[178:179] op_sel_hi:[1,0]
	v_pk_fma_f32 v[194:195], v[72:73], v[178:179], v[194:195] op_sel:[0,1,0] op_sel_hi:[1,1,1]
	v_pk_fma_f32 v[194:195], v[74:75], v[180:181], v[194:195] op_sel_hi:[1,0,1]
	v_pk_fma_f32 v[194:195], v[76:77], v[180:181], v[194:195] op_sel:[0,1,0] op_sel_hi:[1,1,1]

	s_waitcnt lgkmcnt(0)
	ds_read_b128 v[162:165], v79 offset:0x900
	ds_read_b128 v[166:169], v79 offset:0x2900
	ds_read_b128 v[170:173], v79 offset:0x4900
	ds_read_b128 v[174:177], v79 offset:0x6900
	ds_read_b128 v[178:181], v79 offset:0x8900
	ds_read_b64 v[182:183], v198 offset:2304
	v_pk_mul_f32 v[250:251], v[70:71], v[86:87] op_sel_hi:[1,0]
	v_pk_fma_f32 v[250:251], v[72:73], v[86:87], v[250:251] op_sel:[0,1,0] op_sel_hi:[1,1,1]
	v_pk_fma_f32 v[250:251], v[74:75], v[88:89], v[250:251] op_sel_hi:[1,0,1]
	v_pk_fma_f32 v[250:251], v[76:77], v[88:89], v[250:251] op_sel:[0,1,0] op_sel_hi:[1,1,1]
	v_pk_mul_f32 v[184:185], v[126:127], v[118:119] op_sel_hi:[1,0]
	v_pk_mul_f32 v[186:187], v[126:127], v[118:119] op_sel:[0,1] op_sel_hi:[1,1]
	v_add_f32_dpp v252, v251, v250 quad_perm:[1,0,3,2] row_mask:0xf bank_mask:0xf bound_ctrl:1
	v_add_f32_dpp v161, v195, v194 quad_perm:[1,0,3,2] row_mask:0xf bank_mask:0xf bound_ctrl:1
	v_pk_mul_f32 v[188:189], v[126:127], v[120:121] op_sel_hi:[1,0]
	v_add_f32_dpp v252, v252, v252 quad_perm:[2,3,0,1] row_mask:0xf bank_mask:0xf bound_ctrl:1
	v_add_f32_dpp v161, v161, v161 quad_perm:[2,3,0,1] row_mask:0xf bank_mask:0xf bound_ctrl:1
	v_pk_mul_f32 v[190:191], v[126:127], v[120:121] op_sel:[0,1] op_sel_hi:[1,1]
	v_add_f32_dpp v252, v252, v252 row_ror:4 row_mask:0xf bank_mask:0xf bound_ctrl:1
	v_add_f32_dpp v161, v161, v161 row_ror:4 row_mask:0xf bank_mask:0xf bound_ctrl:1
	v_pk_fma_f32 v[184:185], v[70:71], v[82:83], v[184:185] op_sel_hi:[1,0,1]
	v_add_f32_dpp v252, v252, v252 row_ror:8 row_mask:0xf bank_mask:0xf bound_ctrl:1
	v_add_f32_dpp v92, v161, v161 row_ror:8 row_mask:0xf bank_mask:0x8 bound_ctrl:1
	v_pk_fma_f32 v[186:187], v[72:73], v[82:83], v[186:187] op_sel:[0,1,0] op_sel_hi:[1,1,1]
	v_mov_b32_dpp v253, v252 quad_perm:[1,0,3,2] row_mask:0xf bank_mask:0xf bound_ctrl:1
	v_pk_fma_f32 v[188:189], v[74:75], v[84:85], v[188:189] op_sel_hi:[1,0,1]
	v_pk_fma_f32 v[190:191], v[76:77], v[84:85], v[190:191] op_sel:[0,1,0] op_sel_hi:[1,1,1]
	v_pk_fma_f32 v[70:71], v[252:253], v[114:115], v[184:185] op_sel_hi:[1,0,1]
	v_pk_fma_f32 v[72:73], v[252:253], v[114:115], v[186:187] op_sel:[0,1,0] op_sel_hi:[1,1,1]
	v_pk_fma_f32 v[74:75], v[252:253], v[116:117], v[188:189] op_sel_hi:[1,0,1]
	v_pk_fma_f32 v[76:77], v[252:253], v[116:117], v[190:191] op_sel:[0,1,0] op_sel_hi:[1,1,1]
	v_pk_mul_f32 v[192:193], v[70:71], v[122:123] op_sel_hi:[1,0]
	v_pk_fma_f32 v[192:193], v[72:73], v[122:123], v[192:193] op_sel:[0,1,0] op_sel_hi:[1,1,1]
	v_pk_fma_f32 v[192:193], v[74:75], v[124:125], v[192:193] op_sel_hi:[1,0,1]
	v_pk_fma_f32 v[192:193], v[76:77], v[124:125], v[192:193] op_sel:[0,1,0] op_sel_hi:[1,1,1]

	s_nop 0
	ds_write_b32 v197, v92 offset:512
	s_waitcnt lgkmcnt(0)
	s_nop 0
	ds_read_b128 v[82:85], v79 offset:0xa00
	ds_read_b128 v[86:89], v79 offset:0x2a00
	ds_read_b128 v[114:117], v79 offset:0x4a00
	ds_read_b128 v[118:121], v79 offset:0x6a00
	ds_read_b128 v[122:125], v79 offset:0x8a00
	ds_read_b64 v[126:127], v198 offset:2560
	v_pk_mul_f32 v[250:251], v[70:71], v[166:167] op_sel_hi:[1,0]
	v_pk_fma_f32 v[250:251], v[72:73], v[166:167], v[250:251] op_sel:[0,1,0] op_sel_hi:[1,1,1]
	v_pk_fma_f32 v[250:251], v[74:75], v[168:169], v[250:251] op_sel_hi:[1,0,1]
	v_pk_fma_f32 v[250:251], v[76:77], v[168:169], v[250:251] op_sel:[0,1,0] op_sel_hi:[1,1,1]
	v_pk_mul_f32 v[184:185], v[182:183], v[174:175] op_sel_hi:[1,0]
	v_pk_mul_f32 v[186:187], v[182:183], v[174:175] op_sel:[0,1] op_sel_hi:[1,1]
	v_add_f32_dpp v252, v251, v250 quad_perm:[1,0,3,2] row_mask:0xf bank_mask:0xf bound_ctrl:1
	v_add_f32_dpp v92, v193, v192 quad_perm:[1,0,3,2] row_mask:0xf bank_mask:0xf bound_ctrl:1
	v_pk_mul_f32 v[188:189], v[182:183], v[176:177] op_sel_hi:[1,0]
	v_add_f32_dpp v252, v252, v252 quad_perm:[2,3,0,1] row_mask:0xf bank_mask:0xf bound_ctrl:1
	v_add_f32_dpp v92, v92, v92 quad_perm:[2,3,0,1] row_mask:0xf bank_mask:0xf bound_ctrl:1
	v_pk_mul_f32 v[190:191], v[182:183], v[176:177] op_sel:[0,1] op_sel_hi:[1,1]
	v_add_f32_dpp v252, v252, v252 row_ror:4 row_mask:0xf bank_mask:0xf bound_ctrl:1
	v_add_f32_dpp v92, v92, v92 row_ror:4 row_mask:0xf bank_mask:0xf bound_ctrl:1
	v_pk_fma_f32 v[184:185], v[70:71], v[162:163], v[184:185] op_sel_hi:[1,0,1]
	v_add_f32_dpp v252, v252, v252 row_ror:8 row_mask:0xf bank_mask:0xf bound_ctrl:1
	v_add_f32_dpp v92, v92, v92 row_ror:8 row_mask:0xf bank_mask:0x1 bound_ctrl:1
	v_pk_fma_f32 v[186:187], v[72:73], v[162:163], v[186:187] op_sel:[0,1,0] op_sel_hi:[1,1,1]
	v_mov_b32_dpp v253, v252 quad_perm:[1,0,3,2] row_mask:0xf bank_mask:0xf bound_ctrl:1
	v_pk_fma_f32 v[188:189], v[74:75], v[164:165], v[188:189] op_sel_hi:[1,0,1]
	v_pk_fma_f32 v[190:191], v[76:77], v[164:165], v[190:191] op_sel:[0,1,0] op_sel_hi:[1,1,1]
	v_pk_fma_f32 v[70:71], v[252:253], v[170:171], v[184:185] op_sel_hi:[1,0,1]
	v_pk_fma_f32 v[72:73], v[252:253], v[170:171], v[186:187] op_sel:[0,1,0] op_sel_hi:[1,1,1]
	v_pk_fma_f32 v[74:75], v[252:253], v[172:173], v[188:189] op_sel_hi:[1,0,1]
	v_pk_fma_f32 v[76:77], v[252:253], v[172:173], v[190:191] op_sel:[0,1,0] op_sel_hi:[1,1,1]
	v_pk_mul_f32 v[194:195], v[70:71], v[178:179] op_sel_hi:[1,0]
	v_pk_fma_f32 v[194:195], v[72:73], v[178:179], v[194:195] op_sel:[0,1,0] op_sel_hi:[1,1,1]
	v_pk_fma_f32 v[194:195], v[74:75], v[180:181], v[194:195] op_sel_hi:[1,0,1]
	v_pk_fma_f32 v[194:195], v[76:77], v[180:181], v[194:195] op_sel:[0,1,0] op_sel_hi:[1,1,1]

	s_waitcnt lgkmcnt(0)
	ds_read_b128 v[162:165], v79 offset:0xb00
	ds_read_b128 v[166:169], v79 offset:0x2b00
	ds_read_b128 v[170:173], v79 offset:0x4b00
	ds_read_b128 v[174:177], v79 offset:0x6b00
	ds_read_b128 v[178:181], v79 offset:0x8b00
	ds_read_b64 v[182:183], v198 offset:2816
	v_pk_mul_f32 v[250:251], v[70:71], v[86:87] op_sel_hi:[1,0]
	v_pk_fma_f32 v[250:251], v[72:73], v[86:87], v[250:251] op_sel:[0,1,0] op_sel_hi:[1,1,1]
	v_pk_fma_f32 v[250:251], v[74:75], v[88:89], v[250:251] op_sel_hi:[1,0,1]
	v_pk_fma_f32 v[250:251], v[76:77], v[88:89], v[250:251] op_sel:[0,1,0] op_sel_hi:[1,1,1]
	v_pk_mul_f32 v[184:185], v[126:127], v[118:119] op_sel_hi:[1,0]
	v_pk_mul_f32 v[186:187], v[126:127], v[118:119] op_sel:[0,1] op_sel_hi:[1,1]
	v_add_f32_dpp v252, v251, v250 quad_perm:[1,0,3,2] row_mask:0xf bank_mask:0xf bound_ctrl:1
	v_add_f32_dpp v161, v195, v194 quad_perm:[1,0,3,2] row_mask:0xf bank_mask:0xf bound_ctrl:1
	v_pk_mul_f32 v[188:189], v[126:127], v[120:121] op_sel_hi:[1,0]
	v_add_f32_dpp v252, v252, v252 quad_perm:[2,3,0,1] row_mask:0xf bank_mask:0xf bound_ctrl:1
	v_add_f32_dpp v161, v161, v161 quad_perm:[2,3,0,1] row_mask:0xf bank_mask:0xf bound_ctrl:1
	v_pk_mul_f32 v[190:191], v[126:127], v[120:121] op_sel:[0,1] op_sel_hi:[1,1]
	v_add_f32_dpp v252, v252, v252 row_ror:4 row_mask:0xf bank_mask:0xf bound_ctrl:1
	v_add_f32_dpp v161, v161, v161 row_ror:4 row_mask:0xf bank_mask:0xf bound_ctrl:1
	v_pk_fma_f32 v[184:185], v[70:71], v[82:83], v[184:185] op_sel_hi:[1,0,1]
	v_add_f32_dpp v252, v252, v252 row_ror:8 row_mask:0xf bank_mask:0xf bound_ctrl:1
	v_add_f32_dpp v92, v161, v161 row_ror:8 row_mask:0xf bank_mask:0x2 bound_ctrl:1
	v_pk_fma_f32 v[186:187], v[72:73], v[82:83], v[186:187] op_sel:[0,1,0] op_sel_hi:[1,1,1]
	v_mov_b32_dpp v253, v252 quad_perm:[1,0,3,2] row_mask:0xf bank_mask:0xf bound_ctrl:1
	v_pk_fma_f32 v[188:189], v[74:75], v[84:85], v[188:189] op_sel_hi:[1,0,1]
	v_pk_fma_f32 v[190:191], v[76:77], v[84:85], v[190:191] op_sel:[0,1,0] op_sel_hi:[1,1,1]
	v_pk_fma_f32 v[70:71], v[252:253], v[114:115], v[184:185] op_sel_hi:[1,0,1]
	v_pk_fma_f32 v[72:73], v[252:253], v[114:115], v[186:187] op_sel:[0,1,0] op_sel_hi:[1,1,1]
	v_pk_fma_f32 v[74:75], v[252:253], v[116:117], v[188:189] op_sel_hi:[1,0,1]
	v_pk_fma_f32 v[76:77], v[252:253], v[116:117], v[190:191] op_sel:[0,1,0] op_sel_hi:[1,1,1]
	v_pk_mul_f32 v[192:193], v[70:71], v[122:123] op_sel_hi:[1,0]
	v_pk_fma_f32 v[192:193], v[72:73], v[122:123], v[192:193] op_sel:[0,1,0] op_sel_hi:[1,1,1]
	v_pk_fma_f32 v[192:193], v[74:75], v[124:125], v[192:193] op_sel_hi:[1,0,1]
	v_pk_fma_f32 v[192:193], v[76:77], v[124:125], v[192:193] op_sel:[0,1,0] op_sel_hi:[1,1,1]

	s_waitcnt lgkmcnt(0)
	ds_read_b128 v[82:85], v79 offset:0xc00
	ds_read_b128 v[86:89], v79 offset:0x2c00
	ds_read_b128 v[114:117], v79 offset:0x4c00
	ds_read_b128 v[118:121], v79 offset:0x6c00
	ds_read_b128 v[122:125], v79 offset:0x8c00
	ds_read_b64 v[126:127], v198 offset:3072
	v_pk_mul_f32 v[250:251], v[70:71], v[166:167] op_sel_hi:[1,0]
	v_pk_fma_f32 v[250:251], v[72:73], v[166:167], v[250:251] op_sel:[0,1,0] op_sel_hi:[1,1,1]
	v_pk_fma_f32 v[250:251], v[74:75], v[168:169], v[250:251] op_sel_hi:[1,0,1]
	v_pk_fma_f32 v[250:251], v[76:77], v[168:169], v[250:251] op_sel:[0,1,0] op_sel_hi:[1,1,1]
	v_pk_mul_f32 v[184:185], v[182:183], v[174:175] op_sel_hi:[1,0]
	v_pk_mul_f32 v[186:187], v[182:183], v[174:175] op_sel:[0,1] op_sel_hi:[1,1]
	v_add_f32_dpp v252, v251, v250 quad_perm:[1,0,3,2] row_mask:0xf bank_mask:0xf bound_ctrl:1
	v_add_f32_dpp v161, v193, v192 quad_perm:[1,0,3,2] row_mask:0xf bank_mask:0xf bound_ctrl:1
	v_pk_mul_f32 v[188:189], v[182:183], v[176:177] op_sel_hi:[1,0]
	v_add_f32_dpp v252, v252, v252 quad_perm:[2,3,0,1] row_mask:0xf bank_mask:0xf bound_ctrl:1
	v_add_f32_dpp v161, v161, v161 quad_perm:[2,3,0,1] row_mask:0xf bank_mask:0xf bound_ctrl:1
	v_pk_mul_f32 v[190:191], v[182:183], v[176:177] op_sel:[0,1] op_sel_hi:[1,1]
	v_add_f32_dpp v252, v252, v252 row_ror:4 row_mask:0xf bank_mask:0xf bound_ctrl:1
	v_add_f32_dpp v161, v161, v161 row_ror:4 row_mask:0xf bank_mask:0xf bound_ctrl:1
	v_pk_fma_f32 v[184:185], v[70:71], v[162:163], v[184:185] op_sel_hi:[1,0,1]
	v_add_f32_dpp v252, v252, v252 row_ror:8 row_mask:0xf bank_mask:0xf bound_ctrl:1
	v_add_f32_dpp v92, v161, v161 row_ror:8 row_mask:0xf bank_mask:0x4 bound_ctrl:1
	v_pk_fma_f32 v[186:187], v[72:73], v[162:163], v[186:187] op_sel:[0,1,0] op_sel_hi:[1,1,1]
	v_mov_b32_dpp v253, v252 quad_perm:[1,0,3,2] row_mask:0xf bank_mask:0xf bound_ctrl:1
	v_pk_fma_f32 v[188:189], v[74:75], v[164:165], v[188:189] op_sel_hi:[1,0,1]
	v_pk_fma_f32 v[190:191], v[76:77], v[164:165], v[190:191] op_sel:[0,1,0] op_sel_hi:[1,1,1]
	v_pk_fma_f32 v[70:71], v[252:253], v[170:171], v[184:185] op_sel_hi:[1,0,1]
	v_pk_fma_f32 v[72:73], v[252:253], v[170:171], v[186:187] op_sel:[0,1,0] op_sel_hi:[1,1,1]
	v_pk_fma_f32 v[74:75], v[252:253], v[172:173], v[188:189] op_sel_hi:[1,0,1]
	v_pk_fma_f32 v[76:77], v[252:253], v[172:173], v[190:191] op_sel:[0,1,0] op_sel_hi:[1,1,1]
	v_pk_mul_f32 v[194:195], v[70:71], v[178:179] op_sel_hi:[1,0]
	v_pk_fma_f32 v[194:195], v[72:73], v[178:179], v[194:195] op_sel:[0,1,0] op_sel_hi:[1,1,1]
	v_pk_fma_f32 v[194:195], v[74:75], v[180:181], v[194:195] op_sel_hi:[1,0,1]
	v_pk_fma_f32 v[194:195], v[76:77], v[180:181], v[194:195] op_sel:[0,1,0] op_sel_hi:[1,1,1]

	s_waitcnt lgkmcnt(0)
	ds_read_b128 v[162:165], v79 offset:0xd00
	ds_read_b128 v[166:169], v79 offset:0x2d00
	ds_read_b128 v[170:173], v79 offset:0x4d00
	ds_read_b128 v[174:177], v79 offset:0x6d00
	ds_read_b128 v[178:181], v79 offset:0x8d00
	ds_read_b64 v[182:183], v198 offset:3328
	v_pk_mul_f32 v[250:251], v[70:71], v[86:87] op_sel_hi:[1,0]
	v_pk_fma_f32 v[250:251], v[72:73], v[86:87], v[250:251] op_sel:[0,1,0] op_sel_hi:[1,1,1]
	v_pk_fma_f32 v[250:251], v[74:75], v[88:89], v[250:251] op_sel_hi:[1,0,1]
	v_pk_fma_f32 v[250:251], v[76:77], v[88:89], v[250:251] op_sel:[0,1,0] op_sel_hi:[1,1,1]
	v_pk_mul_f32 v[184:185], v[126:127], v[118:119] op_sel_hi:[1,0]
	v_pk_mul_f32 v[186:187], v[126:127], v[118:119] op_sel:[0,1] op_sel_hi:[1,1]
	v_add_f32_dpp v252, v251, v250 quad_perm:[1,0,3,2] row_mask:0xf bank_mask:0xf bound_ctrl:1
	v_add_f32_dpp v161, v195, v194 quad_perm:[1,0,3,2] row_mask:0xf bank_mask:0xf bound_ctrl:1
	v_pk_mul_f32 v[188:189], v[126:127], v[120:121] op_sel_hi:[1,0]
	v_add_f32_dpp v252, v252, v252 quad_perm:[2,3,0,1] row_mask:0xf bank_mask:0xf bound_ctrl:1
	v_add_f32_dpp v161, v161, v161 quad_perm:[2,3,0,1] row_mask:0xf bank_mask:0xf bound_ctrl:1
	v_pk_mul_f32 v[190:191], v[126:127], v[120:121] op_sel:[0,1] op_sel_hi:[1,1]
	v_add_f32_dpp v252, v252, v252 row_ror:4 row_mask:0xf bank_mask:0xf bound_ctrl:1
	v_add_f32_dpp v161, v161, v161 row_ror:4 row_mask:0xf bank_mask:0xf bound_ctrl:1
	v_pk_fma_f32 v[184:185], v[70:71], v[82:83], v[184:185] op_sel_hi:[1,0,1]
	v_add_f32_dpp v252, v252, v252 row_ror:8 row_mask:0xf bank_mask:0xf bound_ctrl:1
	v_add_f32_dpp v92, v161, v161 row_ror:8 row_mask:0xf bank_mask:0x8 bound_ctrl:1
	v_pk_fma_f32 v[186:187], v[72:73], v[82:83], v[186:187] op_sel:[0,1,0] op_sel_hi:[1,1,1]
	v_mov_b32_dpp v253, v252 quad_perm:[1,0,3,2] row_mask:0xf bank_mask:0xf bound_ctrl:1
	v_pk_fma_f32 v[188:189], v[74:75], v[84:85], v[188:189] op_sel_hi:[1,0,1]
	v_pk_fma_f32 v[190:191], v[76:77], v[84:85], v[190:191] op_sel:[0,1,0] op_sel_hi:[1,1,1]
	v_pk_fma_f32 v[70:71], v[252:253], v[114:115], v[184:185] op_sel_hi:[1,0,1]
	v_pk_fma_f32 v[72:73], v[252:253], v[114:115], v[186:187] op_sel:[0,1,0] op_sel_hi:[1,1,1]
	v_pk_fma_f32 v[74:75], v[252:253], v[116:117], v[188:189] op_sel_hi:[1,0,1]
	v_pk_fma_f32 v[76:77], v[252:253], v[116:117], v[190:191] op_sel:[0,1,0] op_sel_hi:[1,1,1]
	v_pk_mul_f32 v[192:193], v[70:71], v[122:123] op_sel_hi:[1,0]
	v_pk_fma_f32 v[192:193], v[72:73], v[122:123], v[192:193] op_sel:[0,1,0] op_sel_hi:[1,1,1]
	v_pk_fma_f32 v[192:193], v[74:75], v[124:125], v[192:193] op_sel_hi:[1,0,1]
	v_pk_fma_f32 v[192:193], v[76:77], v[124:125], v[192:193] op_sel:[0,1,0] op_sel_hi:[1,1,1]

	s_waitcnt lgkmcnt(0)
	ds_write_b32 v197, v92 offset:1024
	ds_read_b128 v[82:85], v79 offset:0xe00
	ds_read_b128 v[86:89], v79 offset:0x2e00
	ds_read_b128 v[114:117], v79 offset:0x4e00
	ds_read_b128 v[118:121], v79 offset:0x6e00
	ds_read_b128 v[122:125], v79 offset:0x8e00
	ds_read_b64 v[126:127], v198 offset:3584
	v_pk_mul_f32 v[250:251], v[70:71], v[166:167] op_sel_hi:[1,0]
	v_pk_fma_f32 v[250:251], v[72:73], v[166:167], v[250:251] op_sel:[0,1,0] op_sel_hi:[1,1,1]
	v_pk_fma_f32 v[250:251], v[74:75], v[168:169], v[250:251] op_sel_hi:[1,0,1]
	v_pk_fma_f32 v[250:251], v[76:77], v[168:169], v[250:251] op_sel:[0,1,0] op_sel_hi:[1,1,1]
	v_pk_mul_f32 v[184:185], v[182:183], v[174:175] op_sel_hi:[1,0]
	v_pk_mul_f32 v[186:187], v[182:183], v[174:175] op_sel:[0,1] op_sel_hi:[1,1]
	v_add_f32_dpp v252, v251, v250 quad_perm:[1,0,3,2] row_mask:0xf bank_mask:0xf bound_ctrl:1
	v_add_f32_dpp v161, v193, v192 quad_perm:[1,0,3,2] row_mask:0xf bank_mask:0xf bound_ctrl:1
	v_pk_mul_f32 v[188:189], v[182:183], v[176:177] op_sel_hi:[1,0]
	v_add_f32_dpp v252, v252, v252 quad_perm:[2,3,0,1] row_mask:0xf bank_mask:0xf bound_ctrl:1
	v_add_f32_dpp v161, v161, v161 quad_perm:[2,3,0,1] row_mask:0xf bank_mask:0xf bound_ctrl:1
	v_pk_mul_f32 v[190:191], v[182:183], v[176:177] op_sel:[0,1] op_sel_hi:[1,1]
	v_add_f32_dpp v252, v252, v252 row_ror:4 row_mask:0xf bank_mask:0xf bound_ctrl:1
	v_add_f32_dpp v161, v161, v161 row_ror:4 row_mask:0xf bank_mask:0xf bound_ctrl:1
	v_pk_fma_f32 v[184:185], v[70:71], v[162:163], v[184:185] op_sel_hi:[1,0,1]
	v_add_f32_dpp v252, v252, v252 row_ror:8 row_mask:0xf bank_mask:0xf bound_ctrl:1
	v_add_f32_dpp v92, v161, v161 row_ror:8 row_mask:0xf bank_mask:0x1 bound_ctrl:1
	v_pk_fma_f32 v[186:187], v[72:73], v[162:163], v[186:187] op_sel:[0,1,0] op_sel_hi:[1,1,1]
	v_mov_b32_dpp v253, v252 quad_perm:[1,0,3,2] row_mask:0xf bank_mask:0xf bound_ctrl:1
	v_pk_fma_f32 v[188:189], v[74:75], v[164:165], v[188:189] op_sel_hi:[1,0,1]
	v_pk_fma_f32 v[190:191], v[76:77], v[164:165], v[190:191] op_sel:[0,1,0] op_sel_hi:[1,1,1]
	v_pk_fma_f32 v[70:71], v[252:253], v[170:171], v[184:185] op_sel_hi:[1,0,1]
	v_pk_fma_f32 v[72:73], v[252:253], v[170:171], v[186:187] op_sel:[0,1,0] op_sel_hi:[1,1,1]
	v_pk_fma_f32 v[74:75], v[252:253], v[172:173], v[188:189] op_sel_hi:[1,0,1]
	v_pk_fma_f32 v[76:77], v[252:253], v[172:173], v[190:191] op_sel:[0,1,0] op_sel_hi:[1,1,1]
	v_pk_mul_f32 v[194:195], v[70:71], v[178:179] op_sel_hi:[1,0]
	v_pk_fma_f32 v[194:195], v[72:73], v[178:179], v[194:195] op_sel:[0,1,0] op_sel_hi:[1,1,1]
	v_pk_fma_f32 v[194:195], v[74:75], v[180:181], v[194:195] op_sel_hi:[1,0,1]
	v_pk_fma_f32 v[194:195], v[76:77], v[180:181], v[194:195] op_sel:[0,1,0] op_sel_hi:[1,1,1]

	s_waitcnt lgkmcnt(0)
	ds_read_b128 v[162:165], v79 offset:0xf00
	ds_read_b128 v[166:169], v79 offset:0x2f00
	ds_read_b128 v[170:173], v79 offset:0x4f00
	ds_read_b128 v[174:177], v79 offset:0x6f00
	ds_read_b128 v[178:181], v79 offset:0x8f00
	ds_read_b64 v[182:183], v198 offset:3840
	v_pk_mul_f32 v[250:251], v[70:71], v[86:87] op_sel_hi:[1,0]
	v_pk_fma_f32 v[250:251], v[72:73], v[86:87], v[250:251] op_sel:[0,1,0] op_sel_hi:[1,1,1]
	v_pk_fma_f32 v[250:251], v[74:75], v[88:89], v[250:251] op_sel_hi:[1,0,1]
	v_pk_fma_f32 v[250:251], v[76:77], v[88:89], v[250:251] op_sel:[0,1,0] op_sel_hi:[1,1,1]
	v_pk_mul_f32 v[184:185], v[126:127], v[118:119] op_sel_hi:[1,0]
	v_pk_mul_f32 v[186:187], v[126:127], v[118:119] op_sel:[0,1] op_sel_hi:[1,1]
	v_add_f32_dpp v252, v251, v250 quad_perm:[1,0,3,2] row_mask:0xf bank_mask:0xf bound_ctrl:1
	v_add_f32_dpp v161, v195, v194 quad_perm:[1,0,3,2] row_mask:0xf bank_mask:0xf bound_ctrl:1
	v_pk_mul_f32 v[188:189], v[126:127], v[120:121] op_sel_hi:[1,0]
	v_add_f32_dpp v252, v252, v252 quad_perm:[2,3,0,1] row_mask:0xf bank_mask:0xf bound_ctrl:1
	v_add_f32_dpp v161, v161, v161 quad_perm:[2,3,0,1] row_mask:0xf bank_mask:0xf bound_ctrl:1
	v_pk_mul_f32 v[190:191], v[126:127], v[120:121] op_sel:[0,1] op_sel_hi:[1,1]
	v_add_f32_dpp v252, v252, v252 row_ror:4 row_mask:0xf bank_mask:0xf bound_ctrl:1
	v_add_f32_dpp v161, v161, v161 row_ror:4 row_mask:0xf bank_mask:0xf bound_ctrl:1
	v_pk_fma_f32 v[184:185], v[70:71], v[82:83], v[184:185] op_sel_hi:[1,0,1]
	v_add_f32_dpp v252, v252, v252 row_ror:8 row_mask:0xf bank_mask:0xf bound_ctrl:1
	v_add_f32_dpp v92, v161, v161 row_ror:8 row_mask:0xf bank_mask:0x2 bound_ctrl:1
	v_pk_fma_f32 v[186:187], v[72:73], v[82:83], v[186:187] op_sel:[0,1,0] op_sel_hi:[1,1,1]
	v_mov_b32_dpp v253, v252 quad_perm:[1,0,3,2] row_mask:0xf bank_mask:0xf bound_ctrl:1
	v_pk_fma_f32 v[188:189], v[74:75], v[84:85], v[188:189] op_sel_hi:[1,0,1]
	v_pk_fma_f32 v[190:191], v[76:77], v[84:85], v[190:191] op_sel:[0,1,0] op_sel_hi:[1,1,1]
	v_pk_fma_f32 v[70:71], v[252:253], v[114:115], v[184:185] op_sel_hi:[1,0,1]
	v_pk_fma_f32 v[72:73], v[252:253], v[114:115], v[186:187] op_sel:[0,1,0] op_sel_hi:[1,1,1]
	v_pk_fma_f32 v[74:75], v[252:253], v[116:117], v[188:189] op_sel_hi:[1,0,1]
	v_pk_fma_f32 v[76:77], v[252:253], v[116:117], v[190:191] op_sel:[0,1,0] op_sel_hi:[1,1,1]
	v_pk_mul_f32 v[192:193], v[70:71], v[122:123] op_sel_hi:[1,0]
	v_pk_fma_f32 v[192:193], v[72:73], v[122:123], v[192:193] op_sel:[0,1,0] op_sel_hi:[1,1,1]
	v_pk_fma_f32 v[192:193], v[74:75], v[124:125], v[192:193] op_sel_hi:[1,0,1]
	v_pk_fma_f32 v[192:193], v[76:77], v[124:125], v[192:193] op_sel:[0,1,0] op_sel_hi:[1,1,1]

	s_waitcnt lgkmcnt(0)
	ds_read_b128 v[82:85], v79 offset:0x1000
	ds_read_b128 v[86:89], v79 offset:0x3000
	ds_read_b128 v[114:117], v79 offset:0x5000
	ds_read_b128 v[118:121], v79 offset:0x7000
	ds_read_b128 v[122:125], v79 offset:0x9000
	ds_read_b64 v[126:127], v198 offset:4096
	v_pk_mul_f32 v[250:251], v[70:71], v[166:167] op_sel_hi:[1,0]
	v_pk_fma_f32 v[250:251], v[72:73], v[166:167], v[250:251] op_sel:[0,1,0] op_sel_hi:[1,1,1]
	v_pk_fma_f32 v[250:251], v[74:75], v[168:169], v[250:251] op_sel_hi:[1,0,1]
	v_pk_fma_f32 v[250:251], v[76:77], v[168:169], v[250:251] op_sel:[0,1,0] op_sel_hi:[1,1,1]
	v_pk_mul_f32 v[184:185], v[182:183], v[174:175] op_sel_hi:[1,0]
	v_pk_mul_f32 v[186:187], v[182:183], v[174:175] op_sel:[0,1] op_sel_hi:[1,1]
	v_add_f32_dpp v252, v251, v250 quad_perm:[1,0,3,2] row_mask:0xf bank_mask:0xf bound_ctrl:1
	v_add_f32_dpp v161, v193, v192 quad_perm:[1,0,3,2] row_mask:0xf bank_mask:0xf bound_ctrl:1
	v_pk_mul_f32 v[188:189], v[182:183], v[176:177] op_sel_hi:[1,0]
	v_add_f32_dpp v252, v252, v252 quad_perm:[2,3,0,1] row_mask:0xf bank_mask:0xf bound_ctrl:1
	v_add_f32_dpp v161, v161, v161 quad_perm:[2,3,0,1] row_mask:0xf bank_mask:0xf bound_ctrl:1
	v_pk_mul_f32 v[190:191], v[182:183], v[176:177] op_sel:[0,1] op_sel_hi:[1,1]
	v_add_f32_dpp v252, v252, v252 row_ror:4 row_mask:0xf bank_mask:0xf bound_ctrl:1
	v_add_f32_dpp v161, v161, v161 row_ror:4 row_mask:0xf bank_mask:0xf bound_ctrl:1
	v_pk_fma_f32 v[184:185], v[70:71], v[162:163], v[184:185] op_sel_hi:[1,0,1]
	v_add_f32_dpp v252, v252, v252 row_ror:8 row_mask:0xf bank_mask:0xf bound_ctrl:1
	v_add_f32_dpp v92, v161, v161 row_ror:8 row_mask:0xf bank_mask:0x4 bound_ctrl:1
	v_pk_fma_f32 v[186:187], v[72:73], v[162:163], v[186:187] op_sel:[0,1,0] op_sel_hi:[1,1,1]
	v_mov_b32_dpp v253, v252 quad_perm:[1,0,3,2] row_mask:0xf bank_mask:0xf bound_ctrl:1
	v_pk_fma_f32 v[188:189], v[74:75], v[164:165], v[188:189] op_sel_hi:[1,0,1]
	v_pk_fma_f32 v[190:191], v[76:77], v[164:165], v[190:191] op_sel:[0,1,0] op_sel_hi:[1,1,1]
	v_pk_fma_f32 v[70:71], v[252:253], v[170:171], v[184:185] op_sel_hi:[1,0,1]
	v_pk_fma_f32 v[72:73], v[252:253], v[170:171], v[186:187] op_sel:[0,1,0] op_sel_hi:[1,1,1]
	v_pk_fma_f32 v[74:75], v[252:253], v[172:173], v[188:189] op_sel_hi:[1,0,1]
	v_pk_fma_f32 v[76:77], v[252:253], v[172:173], v[190:191] op_sel:[0,1,0] op_sel_hi:[1,1,1]
	v_pk_mul_f32 v[194:195], v[70:71], v[178:179] op_sel_hi:[1,0]
	v_pk_fma_f32 v[194:195], v[72:73], v[178:179], v[194:195] op_sel:[0,1,0] op_sel_hi:[1,1,1]
	v_pk_fma_f32 v[194:195], v[74:75], v[180:181], v[194:195] op_sel_hi:[1,0,1]
	v_pk_fma_f32 v[194:195], v[76:77], v[180:181], v[194:195] op_sel:[0,1,0] op_sel_hi:[1,1,1]

	s_waitcnt lgkmcnt(0)
	ds_read_b128 v[162:165], v79 offset:0x1100
	ds_read_b128 v[166:169], v79 offset:0x3100
	ds_read_b128 v[170:173], v79 offset:0x5100
	ds_read_b128 v[174:177], v79 offset:0x7100
	ds_read_b128 v[178:181], v79 offset:0x9100
	ds_read_b64 v[182:183], v198 offset:4352
	v_pk_mul_f32 v[250:251], v[70:71], v[86:87] op_sel_hi:[1,0]
	v_pk_fma_f32 v[250:251], v[72:73], v[86:87], v[250:251] op_sel:[0,1,0] op_sel_hi:[1,1,1]
	v_pk_fma_f32 v[250:251], v[74:75], v[88:89], v[250:251] op_sel_hi:[1,0,1]
	v_pk_fma_f32 v[250:251], v[76:77], v[88:89], v[250:251] op_sel:[0,1,0] op_sel_hi:[1,1,1]
	v_pk_mul_f32 v[184:185], v[126:127], v[118:119] op_sel_hi:[1,0]
	v_pk_mul_f32 v[186:187], v[126:127], v[118:119] op_sel:[0,1] op_sel_hi:[1,1]
	v_add_f32_dpp v252, v251, v250 quad_perm:[1,0,3,2] row_mask:0xf bank_mask:0xf bound_ctrl:1
	v_add_f32_dpp v161, v195, v194 quad_perm:[1,0,3,2] row_mask:0xf bank_mask:0xf bound_ctrl:1
	v_pk_mul_f32 v[188:189], v[126:127], v[120:121] op_sel_hi:[1,0]
	v_add_f32_dpp v252, v252, v252 quad_perm:[2,3,0,1] row_mask:0xf bank_mask:0xf bound_ctrl:1
	v_add_f32_dpp v161, v161, v161 quad_perm:[2,3,0,1] row_mask:0xf bank_mask:0xf bound_ctrl:1
	v_pk_mul_f32 v[190:191], v[126:127], v[120:121] op_sel:[0,1] op_sel_hi:[1,1]
	v_add_f32_dpp v252, v252, v252 row_ror:4 row_mask:0xf bank_mask:0xf bound_ctrl:1
	v_add_f32_dpp v161, v161, v161 row_ror:4 row_mask:0xf bank_mask:0xf bound_ctrl:1
	v_pk_fma_f32 v[184:185], v[70:71], v[82:83], v[184:185] op_sel_hi:[1,0,1]
	v_add_f32_dpp v252, v252, v252 row_ror:8 row_mask:0xf bank_mask:0xf bound_ctrl:1
	v_add_f32_dpp v92, v161, v161 row_ror:8 row_mask:0xf bank_mask:0x8 bound_ctrl:1
	v_pk_fma_f32 v[186:187], v[72:73], v[82:83], v[186:187] op_sel:[0,1,0] op_sel_hi:[1,1,1]
	v_mov_b32_dpp v253, v252 quad_perm:[1,0,3,2] row_mask:0xf bank_mask:0xf bound_ctrl:1
	v_pk_fma_f32 v[188:189], v[74:75], v[84:85], v[188:189] op_sel_hi:[1,0,1]
	v_pk_fma_f32 v[190:191], v[76:77], v[84:85], v[190:191] op_sel:[0,1,0] op_sel_hi:[1,1,1]
	v_pk_fma_f32 v[70:71], v[252:253], v[114:115], v[184:185] op_sel_hi:[1,0,1]
	v_pk_fma_f32 v[72:73], v[252:253], v[114:115], v[186:187] op_sel:[0,1,0] op_sel_hi:[1,1,1]
	v_pk_fma_f32 v[74:75], v[252:253], v[116:117], v[188:189] op_sel_hi:[1,0,1]
	v_pk_fma_f32 v[76:77], v[252:253], v[116:117], v[190:191] op_sel:[0,1,0] op_sel_hi:[1,1,1]
	v_pk_mul_f32 v[192:193], v[70:71], v[122:123] op_sel_hi:[1,0]
	v_pk_fma_f32 v[192:193], v[72:73], v[122:123], v[192:193] op_sel:[0,1,0] op_sel_hi:[1,1,1]
	v_pk_fma_f32 v[192:193], v[74:75], v[124:125], v[192:193] op_sel_hi:[1,0,1]
	v_pk_fma_f32 v[192:193], v[76:77], v[124:125], v[192:193] op_sel:[0,1,0] op_sel_hi:[1,1,1]

	s_nop 0
	ds_write_b32 v197, v92 offset:1536
	s_waitcnt lgkmcnt(0)
	s_nop 0
	ds_read_b128 v[82:85], v79 offset:0x1200
	ds_read_b128 v[86:89], v79 offset:0x3200
	ds_read_b128 v[114:117], v79 offset:0x5200
	ds_read_b128 v[118:121], v79 offset:0x7200
	ds_read_b128 v[122:125], v79 offset:0x9200
	ds_read_b64 v[126:127], v198 offset:4608
	v_pk_mul_f32 v[250:251], v[70:71], v[166:167] op_sel_hi:[1,0]
	v_pk_fma_f32 v[250:251], v[72:73], v[166:167], v[250:251] op_sel:[0,1,0] op_sel_hi:[1,1,1]
	v_pk_fma_f32 v[250:251], v[74:75], v[168:169], v[250:251] op_sel_hi:[1,0,1]
	v_pk_fma_f32 v[250:251], v[76:77], v[168:169], v[250:251] op_sel:[0,1,0] op_sel_hi:[1,1,1]
	v_pk_mul_f32 v[184:185], v[182:183], v[174:175] op_sel_hi:[1,0]
	v_pk_mul_f32 v[186:187], v[182:183], v[174:175] op_sel:[0,1] op_sel_hi:[1,1]
	v_add_f32_dpp v252, v251, v250 quad_perm:[1,0,3,2] row_mask:0xf bank_mask:0xf bound_ctrl:1
	v_add_f32_dpp v92, v193, v192 quad_perm:[1,0,3,2] row_mask:0xf bank_mask:0xf bound_ctrl:1
	v_pk_mul_f32 v[188:189], v[182:183], v[176:177] op_sel_hi:[1,0]
	v_add_f32_dpp v252, v252, v252 quad_perm:[2,3,0,1] row_mask:0xf bank_mask:0xf bound_ctrl:1
	v_add_f32_dpp v92, v92, v92 quad_perm:[2,3,0,1] row_mask:0xf bank_mask:0xf bound_ctrl:1
	v_pk_mul_f32 v[190:191], v[182:183], v[176:177] op_sel:[0,1] op_sel_hi:[1,1]
	v_add_f32_dpp v252, v252, v252 row_ror:4 row_mask:0xf bank_mask:0xf bound_ctrl:1
	v_add_f32_dpp v92, v92, v92 row_ror:4 row_mask:0xf bank_mask:0xf bound_ctrl:1
	v_pk_fma_f32 v[184:185], v[70:71], v[162:163], v[184:185] op_sel_hi:[1,0,1]
	v_add_f32_dpp v252, v252, v252 row_ror:8 row_mask:0xf bank_mask:0xf bound_ctrl:1
	v_add_f32_dpp v92, v92, v92 row_ror:8 row_mask:0xf bank_mask:0x1 bound_ctrl:1
	v_pk_fma_f32 v[186:187], v[72:73], v[162:163], v[186:187] op_sel:[0,1,0] op_sel_hi:[1,1,1]
	v_mov_b32_dpp v253, v252 quad_perm:[1,0,3,2] row_mask:0xf bank_mask:0xf bound_ctrl:1
	v_pk_fma_f32 v[188:189], v[74:75], v[164:165], v[188:189] op_sel_hi:[1,0,1]
	v_pk_fma_f32 v[190:191], v[76:77], v[164:165], v[190:191] op_sel:[0,1,0] op_sel_hi:[1,1,1]
	v_pk_fma_f32 v[70:71], v[252:253], v[170:171], v[184:185] op_sel_hi:[1,0,1]
	v_pk_fma_f32 v[72:73], v[252:253], v[170:171], v[186:187] op_sel:[0,1,0] op_sel_hi:[1,1,1]
	v_pk_fma_f32 v[74:75], v[252:253], v[172:173], v[188:189] op_sel_hi:[1,0,1]
	v_pk_fma_f32 v[76:77], v[252:253], v[172:173], v[190:191] op_sel:[0,1,0] op_sel_hi:[1,1,1]
	v_pk_mul_f32 v[194:195], v[70:71], v[178:179] op_sel_hi:[1,0]
	v_pk_fma_f32 v[194:195], v[72:73], v[178:179], v[194:195] op_sel:[0,1,0] op_sel_hi:[1,1,1]
	v_pk_fma_f32 v[194:195], v[74:75], v[180:181], v[194:195] op_sel_hi:[1,0,1]
	v_pk_fma_f32 v[194:195], v[76:77], v[180:181], v[194:195] op_sel:[0,1,0] op_sel_hi:[1,1,1]

	s_waitcnt lgkmcnt(0)
	ds_read_b128 v[162:165], v79 offset:0x1300
	ds_read_b128 v[166:169], v79 offset:0x3300
	ds_read_b128 v[170:173], v79 offset:0x5300
	ds_read_b128 v[174:177], v79 offset:0x7300
	ds_read_b128 v[178:181], v79 offset:0x9300
	ds_read_b64 v[182:183], v198 offset:4864
	v_pk_mul_f32 v[250:251], v[70:71], v[86:87] op_sel_hi:[1,0]
	v_pk_fma_f32 v[250:251], v[72:73], v[86:87], v[250:251] op_sel:[0,1,0] op_sel_hi:[1,1,1]
	v_pk_fma_f32 v[250:251], v[74:75], v[88:89], v[250:251] op_sel_hi:[1,0,1]
	v_pk_fma_f32 v[250:251], v[76:77], v[88:89], v[250:251] op_sel:[0,1,0] op_sel_hi:[1,1,1]
	v_pk_mul_f32 v[184:185], v[126:127], v[118:119] op_sel_hi:[1,0]
	v_pk_mul_f32 v[186:187], v[126:127], v[118:119] op_sel:[0,1] op_sel_hi:[1,1]
	v_add_f32_dpp v252, v251, v250 quad_perm:[1,0,3,2] row_mask:0xf bank_mask:0xf bound_ctrl:1
	v_add_f32_dpp v161, v195, v194 quad_perm:[1,0,3,2] row_mask:0xf bank_mask:0xf bound_ctrl:1
	v_pk_mul_f32 v[188:189], v[126:127], v[120:121] op_sel_hi:[1,0]
	v_add_f32_dpp v252, v252, v252 quad_perm:[2,3,0,1] row_mask:0xf bank_mask:0xf bound_ctrl:1
	v_add_f32_dpp v161, v161, v161 quad_perm:[2,3,0,1] row_mask:0xf bank_mask:0xf bound_ctrl:1
	v_pk_mul_f32 v[190:191], v[126:127], v[120:121] op_sel:[0,1] op_sel_hi:[1,1]
	v_add_f32_dpp v252, v252, v252 row_ror:4 row_mask:0xf bank_mask:0xf bound_ctrl:1
	v_add_f32_dpp v161, v161, v161 row_ror:4 row_mask:0xf bank_mask:0xf bound_ctrl:1
	v_pk_fma_f32 v[184:185], v[70:71], v[82:83], v[184:185] op_sel_hi:[1,0,1]
	v_add_f32_dpp v252, v252, v252 row_ror:8 row_mask:0xf bank_mask:0xf bound_ctrl:1
	v_add_f32_dpp v92, v161, v161 row_ror:8 row_mask:0xf bank_mask:0x2 bound_ctrl:1
	v_pk_fma_f32 v[186:187], v[72:73], v[82:83], v[186:187] op_sel:[0,1,0] op_sel_hi:[1,1,1]
	v_mov_b32_dpp v253, v252 quad_perm:[1,0,3,2] row_mask:0xf bank_mask:0xf bound_ctrl:1
	v_pk_fma_f32 v[188:189], v[74:75], v[84:85], v[188:189] op_sel_hi:[1,0,1]
	v_pk_fma_f32 v[190:191], v[76:77], v[84:85], v[190:191] op_sel:[0,1,0] op_sel_hi:[1,1,1]
	v_pk_fma_f32 v[70:71], v[252:253], v[114:115], v[184:185] op_sel_hi:[1,0,1]
	v_pk_fma_f32 v[72:73], v[252:253], v[114:115], v[186:187] op_sel:[0,1,0] op_sel_hi:[1,1,1]
	v_pk_fma_f32 v[74:75], v[252:253], v[116:117], v[188:189] op_sel_hi:[1,0,1]
	v_pk_fma_f32 v[76:77], v[252:253], v[116:117], v[190:191] op_sel:[0,1,0] op_sel_hi:[1,1,1]
	v_pk_mul_f32 v[192:193], v[70:71], v[122:123] op_sel_hi:[1,0]
	v_pk_fma_f32 v[192:193], v[72:73], v[122:123], v[192:193] op_sel:[0,1,0] op_sel_hi:[1,1,1]
	v_pk_fma_f32 v[192:193], v[74:75], v[124:125], v[192:193] op_sel_hi:[1,0,1]
	v_pk_fma_f32 v[192:193], v[76:77], v[124:125], v[192:193] op_sel:[0,1,0] op_sel_hi:[1,1,1]

	s_waitcnt lgkmcnt(0)
	ds_read_b128 v[82:85], v79 offset:0x1400
	ds_read_b128 v[86:89], v79 offset:0x3400
	ds_read_b128 v[114:117], v79 offset:0x5400
	ds_read_b128 v[118:121], v79 offset:0x7400
	ds_read_b128 v[122:125], v79 offset:0x9400
	ds_read_b64 v[126:127], v198 offset:5120
	v_pk_mul_f32 v[250:251], v[70:71], v[166:167] op_sel_hi:[1,0]
	v_pk_fma_f32 v[250:251], v[72:73], v[166:167], v[250:251] op_sel:[0,1,0] op_sel_hi:[1,1,1]
	v_pk_fma_f32 v[250:251], v[74:75], v[168:169], v[250:251] op_sel_hi:[1,0,1]
	v_pk_fma_f32 v[250:251], v[76:77], v[168:169], v[250:251] op_sel:[0,1,0] op_sel_hi:[1,1,1]
	v_pk_mul_f32 v[184:185], v[182:183], v[174:175] op_sel_hi:[1,0]
	v_pk_mul_f32 v[186:187], v[182:183], v[174:175] op_sel:[0,1] op_sel_hi:[1,1]
	v_add_f32_dpp v252, v251, v250 quad_perm:[1,0,3,2] row_mask:0xf bank_mask:0xf bound_ctrl:1
	v_add_f32_dpp v161, v193, v192 quad_perm:[1,0,3,2] row_mask:0xf bank_mask:0xf bound_ctrl:1
	v_pk_mul_f32 v[188:189], v[182:183], v[176:177] op_sel_hi:[1,0]
	v_add_f32_dpp v252, v252, v252 quad_perm:[2,3,0,1] row_mask:0xf bank_mask:0xf bound_ctrl:1
	v_add_f32_dpp v161, v161, v161 quad_perm:[2,3,0,1] row_mask:0xf bank_mask:0xf bound_ctrl:1
	v_pk_mul_f32 v[190:191], v[182:183], v[176:177] op_sel:[0,1] op_sel_hi:[1,1]
	v_add_f32_dpp v252, v252, v252 row_ror:4 row_mask:0xf bank_mask:0xf bound_ctrl:1
	v_add_f32_dpp v161, v161, v161 row_ror:4 row_mask:0xf bank_mask:0xf bound_ctrl:1
	v_pk_fma_f32 v[184:185], v[70:71], v[162:163], v[184:185] op_sel_hi:[1,0,1]
	v_add_f32_dpp v252, v252, v252 row_ror:8 row_mask:0xf bank_mask:0xf bound_ctrl:1
	v_add_f32_dpp v92, v161, v161 row_ror:8 row_mask:0xf bank_mask:0x4 bound_ctrl:1
	v_pk_fma_f32 v[186:187], v[72:73], v[162:163], v[186:187] op_sel:[0,1,0] op_sel_hi:[1,1,1]
	v_mov_b32_dpp v253, v252 quad_perm:[1,0,3,2] row_mask:0xf bank_mask:0xf bound_ctrl:1
	v_pk_fma_f32 v[188:189], v[74:75], v[164:165], v[188:189] op_sel_hi:[1,0,1]
	v_pk_fma_f32 v[190:191], v[76:77], v[164:165], v[190:191] op_sel:[0,1,0] op_sel_hi:[1,1,1]
	v_pk_fma_f32 v[70:71], v[252:253], v[170:171], v[184:185] op_sel_hi:[1,0,1]
	v_pk_fma_f32 v[72:73], v[252:253], v[170:171], v[186:187] op_sel:[0,1,0] op_sel_hi:[1,1,1]
	v_pk_fma_f32 v[74:75], v[252:253], v[172:173], v[188:189] op_sel_hi:[1,0,1]
	v_pk_fma_f32 v[76:77], v[252:253], v[172:173], v[190:191] op_sel:[0,1,0] op_sel_hi:[1,1,1]
	v_pk_mul_f32 v[194:195], v[70:71], v[178:179] op_sel_hi:[1,0]
	v_pk_fma_f32 v[194:195], v[72:73], v[178:179], v[194:195] op_sel:[0,1,0] op_sel_hi:[1,1,1]
	v_pk_fma_f32 v[194:195], v[74:75], v[180:181], v[194:195] op_sel_hi:[1,0,1]
	v_pk_fma_f32 v[194:195], v[76:77], v[180:181], v[194:195] op_sel:[0,1,0] op_sel_hi:[1,1,1]

	s_waitcnt lgkmcnt(0)
	ds_read_b128 v[162:165], v79 offset:0x1500
	ds_read_b128 v[166:169], v79 offset:0x3500
	ds_read_b128 v[170:173], v79 offset:0x5500
	ds_read_b128 v[174:177], v79 offset:0x7500
	ds_read_b128 v[178:181], v79 offset:0x9500
	ds_read_b64 v[182:183], v198 offset:5376
	v_pk_mul_f32 v[250:251], v[70:71], v[86:87] op_sel_hi:[1,0]
	v_pk_fma_f32 v[250:251], v[72:73], v[86:87], v[250:251] op_sel:[0,1,0] op_sel_hi:[1,1,1]
	v_pk_fma_f32 v[250:251], v[74:75], v[88:89], v[250:251] op_sel_hi:[1,0,1]
	v_pk_fma_f32 v[250:251], v[76:77], v[88:89], v[250:251] op_sel:[0,1,0] op_sel_hi:[1,1,1]
	v_pk_mul_f32 v[184:185], v[126:127], v[118:119] op_sel_hi:[1,0]
	v_pk_mul_f32 v[186:187], v[126:127], v[118:119] op_sel:[0,1] op_sel_hi:[1,1]
	v_add_f32_dpp v252, v251, v250 quad_perm:[1,0,3,2] row_mask:0xf bank_mask:0xf bound_ctrl:1
	v_add_f32_dpp v161, v195, v194 quad_perm:[1,0,3,2] row_mask:0xf bank_mask:0xf bound_ctrl:1
	v_pk_mul_f32 v[188:189], v[126:127], v[120:121] op_sel_hi:[1,0]
	v_add_f32_dpp v252, v252, v252 quad_perm:[2,3,0,1] row_mask:0xf bank_mask:0xf bound_ctrl:1
	v_add_f32_dpp v161, v161, v161 quad_perm:[2,3,0,1] row_mask:0xf bank_mask:0xf bound_ctrl:1
	v_pk_mul_f32 v[190:191], v[126:127], v[120:121] op_sel:[0,1] op_sel_hi:[1,1]
	v_add_f32_dpp v252, v252, v252 row_ror:4 row_mask:0xf bank_mask:0xf bound_ctrl:1
	v_add_f32_dpp v161, v161, v161 row_ror:4 row_mask:0xf bank_mask:0xf bound_ctrl:1
	v_pk_fma_f32 v[184:185], v[70:71], v[82:83], v[184:185] op_sel_hi:[1,0,1]
	v_add_f32_dpp v252, v252, v252 row_ror:8 row_mask:0xf bank_mask:0xf bound_ctrl:1
	v_add_f32_dpp v92, v161, v161 row_ror:8 row_mask:0xf bank_mask:0x8 bound_ctrl:1
	v_pk_fma_f32 v[186:187], v[72:73], v[82:83], v[186:187] op_sel:[0,1,0] op_sel_hi:[1,1,1]
	v_mov_b32_dpp v253, v252 quad_perm:[1,0,3,2] row_mask:0xf bank_mask:0xf bound_ctrl:1
	v_pk_fma_f32 v[188:189], v[74:75], v[84:85], v[188:189] op_sel_hi:[1,0,1]
	v_pk_fma_f32 v[190:191], v[76:77], v[84:85], v[190:191] op_sel:[0,1,0] op_sel_hi:[1,1,1]
	v_pk_fma_f32 v[70:71], v[252:253], v[114:115], v[184:185] op_sel_hi:[1,0,1]
	v_pk_fma_f32 v[72:73], v[252:253], v[114:115], v[186:187] op_sel:[0,1,0] op_sel_hi:[1,1,1]
	v_pk_fma_f32 v[74:75], v[252:253], v[116:117], v[188:189] op_sel_hi:[1,0,1]
	v_pk_fma_f32 v[76:77], v[252:253], v[116:117], v[190:191] op_sel:[0,1,0] op_sel_hi:[1,1,1]
	v_pk_mul_f32 v[192:193], v[70:71], v[122:123] op_sel_hi:[1,0]
	v_pk_fma_f32 v[192:193], v[72:73], v[122:123], v[192:193] op_sel:[0,1,0] op_sel_hi:[1,1,1]
	v_pk_fma_f32 v[192:193], v[74:75], v[124:125], v[192:193] op_sel_hi:[1,0,1]
	v_pk_fma_f32 v[192:193], v[76:77], v[124:125], v[192:193] op_sel:[0,1,0] op_sel_hi:[1,1,1]

	s_waitcnt lgkmcnt(0)
	ds_write_b32 v197, v92 offset:2048
	ds_read_b128 v[82:85], v79 offset:0x1600
	ds_read_b128 v[86:89], v79 offset:0x3600
	ds_read_b128 v[114:117], v79 offset:0x5600
	ds_read_b128 v[118:121], v79 offset:0x7600
	ds_read_b128 v[122:125], v79 offset:0x9600
	ds_read_b64 v[126:127], v198 offset:5632
	v_pk_mul_f32 v[250:251], v[70:71], v[166:167] op_sel_hi:[1,0]
	v_pk_fma_f32 v[250:251], v[72:73], v[166:167], v[250:251] op_sel:[0,1,0] op_sel_hi:[1,1,1]
	v_pk_fma_f32 v[250:251], v[74:75], v[168:169], v[250:251] op_sel_hi:[1,0,1]
	v_pk_fma_f32 v[250:251], v[76:77], v[168:169], v[250:251] op_sel:[0,1,0] op_sel_hi:[1,1,1]
	v_pk_mul_f32 v[184:185], v[182:183], v[174:175] op_sel_hi:[1,0]
	v_pk_mul_f32 v[186:187], v[182:183], v[174:175] op_sel:[0,1] op_sel_hi:[1,1]
	v_add_f32_dpp v252, v251, v250 quad_perm:[1,0,3,2] row_mask:0xf bank_mask:0xf bound_ctrl:1
	v_add_f32_dpp v161, v193, v192 quad_perm:[1,0,3,2] row_mask:0xf bank_mask:0xf bound_ctrl:1
	v_pk_mul_f32 v[188:189], v[182:183], v[176:177] op_sel_hi:[1,0]
	v_add_f32_dpp v252, v252, v252 quad_perm:[2,3,0,1] row_mask:0xf bank_mask:0xf bound_ctrl:1
	v_add_f32_dpp v161, v161, v161 quad_perm:[2,3,0,1] row_mask:0xf bank_mask:0xf bound_ctrl:1
	v_pk_mul_f32 v[190:191], v[182:183], v[176:177] op_sel:[0,1] op_sel_hi:[1,1]
	v_add_f32_dpp v252, v252, v252 row_ror:4 row_mask:0xf bank_mask:0xf bound_ctrl:1
	v_add_f32_dpp v161, v161, v161 row_ror:4 row_mask:0xf bank_mask:0xf bound_ctrl:1
	v_pk_fma_f32 v[184:185], v[70:71], v[162:163], v[184:185] op_sel_hi:[1,0,1]
	v_add_f32_dpp v252, v252, v252 row_ror:8 row_mask:0xf bank_mask:0xf bound_ctrl:1
	v_add_f32_dpp v92, v161, v161 row_ror:8 row_mask:0xf bank_mask:0x1 bound_ctrl:1
	v_pk_fma_f32 v[186:187], v[72:73], v[162:163], v[186:187] op_sel:[0,1,0] op_sel_hi:[1,1,1]
	v_mov_b32_dpp v253, v252 quad_perm:[1,0,3,2] row_mask:0xf bank_mask:0xf bound_ctrl:1
	v_pk_fma_f32 v[188:189], v[74:75], v[164:165], v[188:189] op_sel_hi:[1,0,1]
	v_pk_fma_f32 v[190:191], v[76:77], v[164:165], v[190:191] op_sel:[0,1,0] op_sel_hi:[1,1,1]
	v_pk_fma_f32 v[70:71], v[252:253], v[170:171], v[184:185] op_sel_hi:[1,0,1]
	v_pk_fma_f32 v[72:73], v[252:253], v[170:171], v[186:187] op_sel:[0,1,0] op_sel_hi:[1,1,1]
	v_pk_fma_f32 v[74:75], v[252:253], v[172:173], v[188:189] op_sel_hi:[1,0,1]
	v_pk_fma_f32 v[76:77], v[252:253], v[172:173], v[190:191] op_sel:[0,1,0] op_sel_hi:[1,1,1]
	v_pk_mul_f32 v[194:195], v[70:71], v[178:179] op_sel_hi:[1,0]
	v_pk_fma_f32 v[194:195], v[72:73], v[178:179], v[194:195] op_sel:[0,1,0] op_sel_hi:[1,1,1]
	v_pk_fma_f32 v[194:195], v[74:75], v[180:181], v[194:195] op_sel_hi:[1,0,1]
	v_pk_fma_f32 v[194:195], v[76:77], v[180:181], v[194:195] op_sel:[0,1,0] op_sel_hi:[1,1,1]

	s_waitcnt lgkmcnt(0)
	ds_read_b128 v[162:165], v79 offset:0x1700
	ds_read_b128 v[166:169], v79 offset:0x3700
	ds_read_b128 v[170:173], v79 offset:0x5700
	ds_read_b128 v[174:177], v79 offset:0x7700
	ds_read_b128 v[178:181], v79 offset:0x9700
	ds_read_b64 v[182:183], v198 offset:5888
	v_pk_mul_f32 v[250:251], v[70:71], v[86:87] op_sel_hi:[1,0]
	v_pk_fma_f32 v[250:251], v[72:73], v[86:87], v[250:251] op_sel:[0,1,0] op_sel_hi:[1,1,1]
	v_pk_fma_f32 v[250:251], v[74:75], v[88:89], v[250:251] op_sel_hi:[1,0,1]
	v_pk_fma_f32 v[250:251], v[76:77], v[88:89], v[250:251] op_sel:[0,1,0] op_sel_hi:[1,1,1]
	v_pk_mul_f32 v[184:185], v[126:127], v[118:119] op_sel_hi:[1,0]
	v_pk_mul_f32 v[186:187], v[126:127], v[118:119] op_sel:[0,1] op_sel_hi:[1,1]
	v_add_f32_dpp v252, v251, v250 quad_perm:[1,0,3,2] row_mask:0xf bank_mask:0xf bound_ctrl:1
	v_add_f32_dpp v161, v195, v194 quad_perm:[1,0,3,2] row_mask:0xf bank_mask:0xf bound_ctrl:1
	v_pk_mul_f32 v[188:189], v[126:127], v[120:121] op_sel_hi:[1,0]
	v_add_f32_dpp v252, v252, v252 quad_perm:[2,3,0,1] row_mask:0xf bank_mask:0xf bound_ctrl:1
	v_add_f32_dpp v161, v161, v161 quad_perm:[2,3,0,1] row_mask:0xf bank_mask:0xf bound_ctrl:1
	v_pk_mul_f32 v[190:191], v[126:127], v[120:121] op_sel:[0,1] op_sel_hi:[1,1]
	v_add_f32_dpp v252, v252, v252 row_ror:4 row_mask:0xf bank_mask:0xf bound_ctrl:1
	v_add_f32_dpp v161, v161, v161 row_ror:4 row_mask:0xf bank_mask:0xf bound_ctrl:1
	v_pk_fma_f32 v[184:185], v[70:71], v[82:83], v[184:185] op_sel_hi:[1,0,1]
	v_add_f32_dpp v252, v252, v252 row_ror:8 row_mask:0xf bank_mask:0xf bound_ctrl:1
	v_add_f32_dpp v92, v161, v161 row_ror:8 row_mask:0xf bank_mask:0x2 bound_ctrl:1
	v_pk_fma_f32 v[186:187], v[72:73], v[82:83], v[186:187] op_sel:[0,1,0] op_sel_hi:[1,1,1]
	v_mov_b32_dpp v253, v252 quad_perm:[1,0,3,2] row_mask:0xf bank_mask:0xf bound_ctrl:1
	v_pk_fma_f32 v[188:189], v[74:75], v[84:85], v[188:189] op_sel_hi:[1,0,1]
	v_pk_fma_f32 v[190:191], v[76:77], v[84:85], v[190:191] op_sel:[0,1,0] op_sel_hi:[1,1,1]
	v_pk_fma_f32 v[70:71], v[252:253], v[114:115], v[184:185] op_sel_hi:[1,0,1]
	v_pk_fma_f32 v[72:73], v[252:253], v[114:115], v[186:187] op_sel:[0,1,0] op_sel_hi:[1,1,1]
	v_pk_fma_f32 v[74:75], v[252:253], v[116:117], v[188:189] op_sel_hi:[1,0,1]
	v_pk_fma_f32 v[76:77], v[252:253], v[116:117], v[190:191] op_sel:[0,1,0] op_sel_hi:[1,1,1]
	v_pk_mul_f32 v[192:193], v[70:71], v[122:123] op_sel_hi:[1,0]
	v_pk_fma_f32 v[192:193], v[72:73], v[122:123], v[192:193] op_sel:[0,1,0] op_sel_hi:[1,1,1]
	v_pk_fma_f32 v[192:193], v[74:75], v[124:125], v[192:193] op_sel_hi:[1,0,1]
	v_pk_fma_f32 v[192:193], v[76:77], v[124:125], v[192:193] op_sel:[0,1,0] op_sel_hi:[1,1,1]

	s_waitcnt lgkmcnt(0)
	ds_read_b128 v[82:85], v79 offset:0x1800
	ds_read_b128 v[86:89], v79 offset:0x3800
	ds_read_b128 v[114:117], v79 offset:0x5800
	ds_read_b128 v[118:121], v79 offset:0x7800
	ds_read_b128 v[122:125], v79 offset:0x9800
	ds_read_b64 v[126:127], v198 offset:6144
	v_pk_mul_f32 v[250:251], v[70:71], v[166:167] op_sel_hi:[1,0]
	v_pk_fma_f32 v[250:251], v[72:73], v[166:167], v[250:251] op_sel:[0,1,0] op_sel_hi:[1,1,1]
	v_pk_fma_f32 v[250:251], v[74:75], v[168:169], v[250:251] op_sel_hi:[1,0,1]
	v_pk_fma_f32 v[250:251], v[76:77], v[168:169], v[250:251] op_sel:[0,1,0] op_sel_hi:[1,1,1]
	v_pk_mul_f32 v[184:185], v[182:183], v[174:175] op_sel_hi:[1,0]
	v_pk_mul_f32 v[186:187], v[182:183], v[174:175] op_sel:[0,1] op_sel_hi:[1,1]
	v_add_f32_dpp v252, v251, v250 quad_perm:[1,0,3,2] row_mask:0xf bank_mask:0xf bound_ctrl:1
	v_add_f32_dpp v161, v193, v192 quad_perm:[1,0,3,2] row_mask:0xf bank_mask:0xf bound_ctrl:1
	v_pk_mul_f32 v[188:189], v[182:183], v[176:177] op_sel_hi:[1,0]
	v_add_f32_dpp v252, v252, v252 quad_perm:[2,3,0,1] row_mask:0xf bank_mask:0xf bound_ctrl:1
	v_add_f32_dpp v161, v161, v161 quad_perm:[2,3,0,1] row_mask:0xf bank_mask:0xf bound_ctrl:1
	v_pk_mul_f32 v[190:191], v[182:183], v[176:177] op_sel:[0,1] op_sel_hi:[1,1]
	v_add_f32_dpp v252, v252, v252 row_ror:4 row_mask:0xf bank_mask:0xf bound_ctrl:1
	v_add_f32_dpp v161, v161, v161 row_ror:4 row_mask:0xf bank_mask:0xf bound_ctrl:1
	v_pk_fma_f32 v[184:185], v[70:71], v[162:163], v[184:185] op_sel_hi:[1,0,1]
	v_add_f32_dpp v252, v252, v252 row_ror:8 row_mask:0xf bank_mask:0xf bound_ctrl:1
	v_add_f32_dpp v92, v161, v161 row_ror:8 row_mask:0xf bank_mask:0x4 bound_ctrl:1
	v_pk_fma_f32 v[186:187], v[72:73], v[162:163], v[186:187] op_sel:[0,1,0] op_sel_hi:[1,1,1]
	v_mov_b32_dpp v253, v252 quad_perm:[1,0,3,2] row_mask:0xf bank_mask:0xf bound_ctrl:1
	v_pk_fma_f32 v[188:189], v[74:75], v[164:165], v[188:189] op_sel_hi:[1,0,1]
	v_pk_fma_f32 v[190:191], v[76:77], v[164:165], v[190:191] op_sel:[0,1,0] op_sel_hi:[1,1,1]
	v_pk_fma_f32 v[70:71], v[252:253], v[170:171], v[184:185] op_sel_hi:[1,0,1]
	v_pk_fma_f32 v[72:73], v[252:253], v[170:171], v[186:187] op_sel:[0,1,0] op_sel_hi:[1,1,1]
	v_pk_fma_f32 v[74:75], v[252:253], v[172:173], v[188:189] op_sel_hi:[1,0,1]
	v_pk_fma_f32 v[76:77], v[252:253], v[172:173], v[190:191] op_sel:[0,1,0] op_sel_hi:[1,1,1]
	v_pk_mul_f32 v[194:195], v[70:71], v[178:179] op_sel_hi:[1,0]
	v_pk_fma_f32 v[194:195], v[72:73], v[178:179], v[194:195] op_sel:[0,1,0] op_sel_hi:[1,1,1]
	v_pk_fma_f32 v[194:195], v[74:75], v[180:181], v[194:195] op_sel_hi:[1,0,1]
	v_pk_fma_f32 v[194:195], v[76:77], v[180:181], v[194:195] op_sel:[0,1,0] op_sel_hi:[1,1,1]

	s_waitcnt lgkmcnt(0)
	ds_read_b128 v[162:165], v79 offset:0x1900
	ds_read_b128 v[166:169], v79 offset:0x3900
	ds_read_b128 v[170:173], v79 offset:0x5900
	ds_read_b128 v[174:177], v79 offset:0x7900
	ds_read_b128 v[178:181], v79 offset:0x9900
	ds_read_b64 v[182:183], v198 offset:6400
	v_pk_mul_f32 v[250:251], v[70:71], v[86:87] op_sel_hi:[1,0]
	v_pk_fma_f32 v[250:251], v[72:73], v[86:87], v[250:251] op_sel:[0,1,0] op_sel_hi:[1,1,1]
	v_pk_fma_f32 v[250:251], v[74:75], v[88:89], v[250:251] op_sel_hi:[1,0,1]
	v_pk_fma_f32 v[250:251], v[76:77], v[88:89], v[250:251] op_sel:[0,1,0] op_sel_hi:[1,1,1]
	v_pk_mul_f32 v[184:185], v[126:127], v[118:119] op_sel_hi:[1,0]
	v_pk_mul_f32 v[186:187], v[126:127], v[118:119] op_sel:[0,1] op_sel_hi:[1,1]
	v_add_f32_dpp v252, v251, v250 quad_perm:[1,0,3,2] row_mask:0xf bank_mask:0xf bound_ctrl:1
	v_add_f32_dpp v161, v195, v194 quad_perm:[1,0,3,2] row_mask:0xf bank_mask:0xf bound_ctrl:1
	v_pk_mul_f32 v[188:189], v[126:127], v[120:121] op_sel_hi:[1,0]
	v_add_f32_dpp v252, v252, v252 quad_perm:[2,3,0,1] row_mask:0xf bank_mask:0xf bound_ctrl:1
	v_add_f32_dpp v161, v161, v161 quad_perm:[2,3,0,1] row_mask:0xf bank_mask:0xf bound_ctrl:1
	v_pk_mul_f32 v[190:191], v[126:127], v[120:121] op_sel:[0,1] op_sel_hi:[1,1]
	v_add_f32_dpp v252, v252, v252 row_ror:4 row_mask:0xf bank_mask:0xf bound_ctrl:1
	v_add_f32_dpp v161, v161, v161 row_ror:4 row_mask:0xf bank_mask:0xf bound_ctrl:1
	v_pk_fma_f32 v[184:185], v[70:71], v[82:83], v[184:185] op_sel_hi:[1,0,1]
	v_add_f32_dpp v252, v252, v252 row_ror:8 row_mask:0xf bank_mask:0xf bound_ctrl:1
	v_add_f32_dpp v92, v161, v161 row_ror:8 row_mask:0xf bank_mask:0x8 bound_ctrl:1
	v_pk_fma_f32 v[186:187], v[72:73], v[82:83], v[186:187] op_sel:[0,1,0] op_sel_hi:[1,1,1]
	v_mov_b32_dpp v253, v252 quad_perm:[1,0,3,2] row_mask:0xf bank_mask:0xf bound_ctrl:1
	v_pk_fma_f32 v[188:189], v[74:75], v[84:85], v[188:189] op_sel_hi:[1,0,1]
	v_pk_fma_f32 v[190:191], v[76:77], v[84:85], v[190:191] op_sel:[0,1,0] op_sel_hi:[1,1,1]
	v_pk_fma_f32 v[70:71], v[252:253], v[114:115], v[184:185] op_sel_hi:[1,0,1]
	v_pk_fma_f32 v[72:73], v[252:253], v[114:115], v[186:187] op_sel:[0,1,0] op_sel_hi:[1,1,1]
	v_pk_fma_f32 v[74:75], v[252:253], v[116:117], v[188:189] op_sel_hi:[1,0,1]
	v_pk_fma_f32 v[76:77], v[252:253], v[116:117], v[190:191] op_sel:[0,1,0] op_sel_hi:[1,1,1]
	v_pk_mul_f32 v[192:193], v[70:71], v[122:123] op_sel_hi:[1,0]
	v_pk_fma_f32 v[192:193], v[72:73], v[122:123], v[192:193] op_sel:[0,1,0] op_sel_hi:[1,1,1]
	v_pk_fma_f32 v[192:193], v[74:75], v[124:125], v[192:193] op_sel_hi:[1,0,1]
	v_pk_fma_f32 v[192:193], v[76:77], v[124:125], v[192:193] op_sel:[0,1,0] op_sel_hi:[1,1,1]

	s_nop 0
	ds_write_b32 v197, v92 offset:2560
	s_waitcnt lgkmcnt(0)
	s_nop 0
	ds_read_b128 v[82:85], v79 offset:0x1a00
	ds_read_b128 v[86:89], v79 offset:0x3a00
	ds_read_b128 v[114:117], v79 offset:0x5a00
	ds_read_b128 v[118:121], v79 offset:0x7a00
	ds_read_b128 v[122:125], v79 offset:0x9a00
	ds_read_b64 v[126:127], v198 offset:6656
	v_pk_mul_f32 v[250:251], v[70:71], v[166:167] op_sel_hi:[1,0]
	v_pk_fma_f32 v[250:251], v[72:73], v[166:167], v[250:251] op_sel:[0,1,0] op_sel_hi:[1,1,1]
	v_pk_fma_f32 v[250:251], v[74:75], v[168:169], v[250:251] op_sel_hi:[1,0,1]
	v_pk_fma_f32 v[250:251], v[76:77], v[168:169], v[250:251] op_sel:[0,1,0] op_sel_hi:[1,1,1]
	v_pk_mul_f32 v[184:185], v[182:183], v[174:175] op_sel_hi:[1,0]
	v_pk_mul_f32 v[186:187], v[182:183], v[174:175] op_sel:[0,1] op_sel_hi:[1,1]
	v_add_f32_dpp v252, v251, v250 quad_perm:[1,0,3,2] row_mask:0xf bank_mask:0xf bound_ctrl:1
	v_add_f32_dpp v92, v193, v192 quad_perm:[1,0,3,2] row_mask:0xf bank_mask:0xf bound_ctrl:1
	v_pk_mul_f32 v[188:189], v[182:183], v[176:177] op_sel_hi:[1,0]
	v_add_f32_dpp v252, v252, v252 quad_perm:[2,3,0,1] row_mask:0xf bank_mask:0xf bound_ctrl:1
	v_add_f32_dpp v92, v92, v92 quad_perm:[2,3,0,1] row_mask:0xf bank_mask:0xf bound_ctrl:1
	v_pk_mul_f32 v[190:191], v[182:183], v[176:177] op_sel:[0,1] op_sel_hi:[1,1]
	v_add_f32_dpp v252, v252, v252 row_ror:4 row_mask:0xf bank_mask:0xf bound_ctrl:1
	v_add_f32_dpp v92, v92, v92 row_ror:4 row_mask:0xf bank_mask:0xf bound_ctrl:1
	v_pk_fma_f32 v[184:185], v[70:71], v[162:163], v[184:185] op_sel_hi:[1,0,1]
	v_add_f32_dpp v252, v252, v252 row_ror:8 row_mask:0xf bank_mask:0xf bound_ctrl:1
	v_add_f32_dpp v92, v92, v92 row_ror:8 row_mask:0xf bank_mask:0x1 bound_ctrl:1
	v_pk_fma_f32 v[186:187], v[72:73], v[162:163], v[186:187] op_sel:[0,1,0] op_sel_hi:[1,1,1]
	v_mov_b32_dpp v253, v252 quad_perm:[1,0,3,2] row_mask:0xf bank_mask:0xf bound_ctrl:1
	v_pk_fma_f32 v[188:189], v[74:75], v[164:165], v[188:189] op_sel_hi:[1,0,1]
	v_pk_fma_f32 v[190:191], v[76:77], v[164:165], v[190:191] op_sel:[0,1,0] op_sel_hi:[1,1,1]
	v_pk_fma_f32 v[70:71], v[252:253], v[170:171], v[184:185] op_sel_hi:[1,0,1]
	v_pk_fma_f32 v[72:73], v[252:253], v[170:171], v[186:187] op_sel:[0,1,0] op_sel_hi:[1,1,1]
	v_pk_fma_f32 v[74:75], v[252:253], v[172:173], v[188:189] op_sel_hi:[1,0,1]
	v_pk_fma_f32 v[76:77], v[252:253], v[172:173], v[190:191] op_sel:[0,1,0] op_sel_hi:[1,1,1]
	v_pk_mul_f32 v[194:195], v[70:71], v[178:179] op_sel_hi:[1,0]
	v_pk_fma_f32 v[194:195], v[72:73], v[178:179], v[194:195] op_sel:[0,1,0] op_sel_hi:[1,1,1]
	v_pk_fma_f32 v[194:195], v[74:75], v[180:181], v[194:195] op_sel_hi:[1,0,1]
	v_pk_fma_f32 v[194:195], v[76:77], v[180:181], v[194:195] op_sel:[0,1,0] op_sel_hi:[1,1,1]

	s_waitcnt lgkmcnt(0)
	ds_read_b128 v[162:165], v79 offset:0x1b00
	ds_read_b128 v[166:169], v79 offset:0x3b00
	ds_read_b128 v[170:173], v79 offset:0x5b00
	ds_read_b128 v[174:177], v79 offset:0x7b00
	ds_read_b128 v[178:181], v79 offset:0x9b00
	ds_read_b64 v[182:183], v198 offset:6912
	v_pk_mul_f32 v[250:251], v[70:71], v[86:87] op_sel_hi:[1,0]
	v_pk_fma_f32 v[250:251], v[72:73], v[86:87], v[250:251] op_sel:[0,1,0] op_sel_hi:[1,1,1]
	v_pk_fma_f32 v[250:251], v[74:75], v[88:89], v[250:251] op_sel_hi:[1,0,1]
	v_pk_fma_f32 v[250:251], v[76:77], v[88:89], v[250:251] op_sel:[0,1,0] op_sel_hi:[1,1,1]
	v_pk_mul_f32 v[184:185], v[126:127], v[118:119] op_sel_hi:[1,0]
	v_pk_mul_f32 v[186:187], v[126:127], v[118:119] op_sel:[0,1] op_sel_hi:[1,1]
	v_add_f32_dpp v252, v251, v250 quad_perm:[1,0,3,2] row_mask:0xf bank_mask:0xf bound_ctrl:1
	v_add_f32_dpp v161, v195, v194 quad_perm:[1,0,3,2] row_mask:0xf bank_mask:0xf bound_ctrl:1
	v_pk_mul_f32 v[188:189], v[126:127], v[120:121] op_sel_hi:[1,0]
	v_add_f32_dpp v252, v252, v252 quad_perm:[2,3,0,1] row_mask:0xf bank_mask:0xf bound_ctrl:1
	v_add_f32_dpp v161, v161, v161 quad_perm:[2,3,0,1] row_mask:0xf bank_mask:0xf bound_ctrl:1
	v_pk_mul_f32 v[190:191], v[126:127], v[120:121] op_sel:[0,1] op_sel_hi:[1,1]
	v_add_f32_dpp v252, v252, v252 row_ror:4 row_mask:0xf bank_mask:0xf bound_ctrl:1
	v_add_f32_dpp v161, v161, v161 row_ror:4 row_mask:0xf bank_mask:0xf bound_ctrl:1
	v_pk_fma_f32 v[184:185], v[70:71], v[82:83], v[184:185] op_sel_hi:[1,0,1]
	v_add_f32_dpp v252, v252, v252 row_ror:8 row_mask:0xf bank_mask:0xf bound_ctrl:1
	v_add_f32_dpp v92, v161, v161 row_ror:8 row_mask:0xf bank_mask:0x2 bound_ctrl:1
	v_pk_fma_f32 v[186:187], v[72:73], v[82:83], v[186:187] op_sel:[0,1,0] op_sel_hi:[1,1,1]
	v_mov_b32_dpp v253, v252 quad_perm:[1,0,3,2] row_mask:0xf bank_mask:0xf bound_ctrl:1
	v_pk_fma_f32 v[188:189], v[74:75], v[84:85], v[188:189] op_sel_hi:[1,0,1]
	v_pk_fma_f32 v[190:191], v[76:77], v[84:85], v[190:191] op_sel:[0,1,0] op_sel_hi:[1,1,1]
	v_pk_fma_f32 v[70:71], v[252:253], v[114:115], v[184:185] op_sel_hi:[1,0,1]
	v_pk_fma_f32 v[72:73], v[252:253], v[114:115], v[186:187] op_sel:[0,1,0] op_sel_hi:[1,1,1]
	v_pk_fma_f32 v[74:75], v[252:253], v[116:117], v[188:189] op_sel_hi:[1,0,1]
	v_pk_fma_f32 v[76:77], v[252:253], v[116:117], v[190:191] op_sel:[0,1,0] op_sel_hi:[1,1,1]
	v_pk_mul_f32 v[192:193], v[70:71], v[122:123] op_sel_hi:[1,0]
	v_pk_fma_f32 v[192:193], v[72:73], v[122:123], v[192:193] op_sel:[0,1,0] op_sel_hi:[1,1,1]
	v_pk_fma_f32 v[192:193], v[74:75], v[124:125], v[192:193] op_sel_hi:[1,0,1]
	v_pk_fma_f32 v[192:193], v[76:77], v[124:125], v[192:193] op_sel:[0,1,0] op_sel_hi:[1,1,1]

	s_waitcnt lgkmcnt(0)
	ds_read_b128 v[82:85], v79 offset:0x1c00
	ds_read_b128 v[86:89], v79 offset:0x3c00
	ds_read_b128 v[114:117], v79 offset:0x5c00
	ds_read_b128 v[118:121], v79 offset:0x7c00
	ds_read_b128 v[122:125], v79 offset:0x9c00
	ds_read_b64 v[126:127], v198 offset:7168
	v_pk_mul_f32 v[250:251], v[70:71], v[166:167] op_sel_hi:[1,0]
	v_pk_fma_f32 v[250:251], v[72:73], v[166:167], v[250:251] op_sel:[0,1,0] op_sel_hi:[1,1,1]
	v_pk_fma_f32 v[250:251], v[74:75], v[168:169], v[250:251] op_sel_hi:[1,0,1]
	v_pk_fma_f32 v[250:251], v[76:77], v[168:169], v[250:251] op_sel:[0,1,0] op_sel_hi:[1,1,1]
	v_pk_mul_f32 v[184:185], v[182:183], v[174:175] op_sel_hi:[1,0]
	v_pk_mul_f32 v[186:187], v[182:183], v[174:175] op_sel:[0,1] op_sel_hi:[1,1]
	v_add_f32_dpp v252, v251, v250 quad_perm:[1,0,3,2] row_mask:0xf bank_mask:0xf bound_ctrl:1
	v_add_f32_dpp v161, v193, v192 quad_perm:[1,0,3,2] row_mask:0xf bank_mask:0xf bound_ctrl:1
	v_pk_mul_f32 v[188:189], v[182:183], v[176:177] op_sel_hi:[1,0]
	v_add_f32_dpp v252, v252, v252 quad_perm:[2,3,0,1] row_mask:0xf bank_mask:0xf bound_ctrl:1
	v_add_f32_dpp v161, v161, v161 quad_perm:[2,3,0,1] row_mask:0xf bank_mask:0xf bound_ctrl:1
	v_pk_mul_f32 v[190:191], v[182:183], v[176:177] op_sel:[0,1] op_sel_hi:[1,1]
	v_add_f32_dpp v252, v252, v252 row_ror:4 row_mask:0xf bank_mask:0xf bound_ctrl:1
	v_add_f32_dpp v161, v161, v161 row_ror:4 row_mask:0xf bank_mask:0xf bound_ctrl:1
	v_pk_fma_f32 v[184:185], v[70:71], v[162:163], v[184:185] op_sel_hi:[1,0,1]
	v_add_f32_dpp v252, v252, v252 row_ror:8 row_mask:0xf bank_mask:0xf bound_ctrl:1
	v_add_f32_dpp v92, v161, v161 row_ror:8 row_mask:0xf bank_mask:0x4 bound_ctrl:1
	v_pk_fma_f32 v[186:187], v[72:73], v[162:163], v[186:187] op_sel:[0,1,0] op_sel_hi:[1,1,1]
	v_mov_b32_dpp v253, v252 quad_perm:[1,0,3,2] row_mask:0xf bank_mask:0xf bound_ctrl:1
	v_pk_fma_f32 v[188:189], v[74:75], v[164:165], v[188:189] op_sel_hi:[1,0,1]
	v_pk_fma_f32 v[190:191], v[76:77], v[164:165], v[190:191] op_sel:[0,1,0] op_sel_hi:[1,1,1]
	v_pk_fma_f32 v[70:71], v[252:253], v[170:171], v[184:185] op_sel_hi:[1,0,1]
	v_pk_fma_f32 v[72:73], v[252:253], v[170:171], v[186:187] op_sel:[0,1,0] op_sel_hi:[1,1,1]
	v_pk_fma_f32 v[74:75], v[252:253], v[172:173], v[188:189] op_sel_hi:[1,0,1]
	v_pk_fma_f32 v[76:77], v[252:253], v[172:173], v[190:191] op_sel:[0,1,0] op_sel_hi:[1,1,1]
	v_pk_mul_f32 v[194:195], v[70:71], v[178:179] op_sel_hi:[1,0]
	v_pk_fma_f32 v[194:195], v[72:73], v[178:179], v[194:195] op_sel:[0,1,0] op_sel_hi:[1,1,1]
	v_pk_fma_f32 v[194:195], v[74:75], v[180:181], v[194:195] op_sel_hi:[1,0,1]
	v_pk_fma_f32 v[194:195], v[76:77], v[180:181], v[194:195] op_sel:[0,1,0] op_sel_hi:[1,1,1]

	s_waitcnt lgkmcnt(0)
	ds_read_b128 v[162:165], v79 offset:0x1d00
	ds_read_b128 v[166:169], v79 offset:0x3d00
	ds_read_b128 v[170:173], v79 offset:0x5d00
	ds_read_b128 v[174:177], v79 offset:0x7d00
	ds_read_b128 v[178:181], v79 offset:0x9d00
	ds_read_b64 v[182:183], v198 offset:7424
	v_pk_mul_f32 v[250:251], v[70:71], v[86:87] op_sel_hi:[1,0]
	v_pk_fma_f32 v[250:251], v[72:73], v[86:87], v[250:251] op_sel:[0,1,0] op_sel_hi:[1,1,1]
	v_pk_fma_f32 v[250:251], v[74:75], v[88:89], v[250:251] op_sel_hi:[1,0,1]
	v_pk_fma_f32 v[250:251], v[76:77], v[88:89], v[250:251] op_sel:[0,1,0] op_sel_hi:[1,1,1]
	v_pk_mul_f32 v[184:185], v[126:127], v[118:119] op_sel_hi:[1,0]
	v_pk_mul_f32 v[186:187], v[126:127], v[118:119] op_sel:[0,1] op_sel_hi:[1,1]
	v_add_f32_dpp v252, v251, v250 quad_perm:[1,0,3,2] row_mask:0xf bank_mask:0xf bound_ctrl:1
	v_add_f32_dpp v161, v195, v194 quad_perm:[1,0,3,2] row_mask:0xf bank_mask:0xf bound_ctrl:1
	v_pk_mul_f32 v[188:189], v[126:127], v[120:121] op_sel_hi:[1,0]
	v_add_f32_dpp v252, v252, v252 quad_perm:[2,3,0,1] row_mask:0xf bank_mask:0xf bound_ctrl:1
	v_add_f32_dpp v161, v161, v161 quad_perm:[2,3,0,1] row_mask:0xf bank_mask:0xf bound_ctrl:1
	v_pk_mul_f32 v[190:191], v[126:127], v[120:121] op_sel:[0,1] op_sel_hi:[1,1]
	v_add_f32_dpp v252, v252, v252 row_ror:4 row_mask:0xf bank_mask:0xf bound_ctrl:1
	v_add_f32_dpp v161, v161, v161 row_ror:4 row_mask:0xf bank_mask:0xf bound_ctrl:1
	v_pk_fma_f32 v[184:185], v[70:71], v[82:83], v[184:185] op_sel_hi:[1,0,1]
	v_add_f32_dpp v252, v252, v252 row_ror:8 row_mask:0xf bank_mask:0xf bound_ctrl:1
	v_add_f32_dpp v92, v161, v161 row_ror:8 row_mask:0xf bank_mask:0x8 bound_ctrl:1
	v_pk_fma_f32 v[186:187], v[72:73], v[82:83], v[186:187] op_sel:[0,1,0] op_sel_hi:[1,1,1]
	v_mov_b32_dpp v253, v252 quad_perm:[1,0,3,2] row_mask:0xf bank_mask:0xf bound_ctrl:1
	v_pk_fma_f32 v[188:189], v[74:75], v[84:85], v[188:189] op_sel_hi:[1,0,1]
	v_pk_fma_f32 v[190:191], v[76:77], v[84:85], v[190:191] op_sel:[0,1,0] op_sel_hi:[1,1,1]
	v_pk_fma_f32 v[70:71], v[252:253], v[114:115], v[184:185] op_sel_hi:[1,0,1]
	v_pk_fma_f32 v[72:73], v[252:253], v[114:115], v[186:187] op_sel:[0,1,0] op_sel_hi:[1,1,1]
	v_pk_fma_f32 v[74:75], v[252:253], v[116:117], v[188:189] op_sel_hi:[1,0,1]
	v_pk_fma_f32 v[76:77], v[252:253], v[116:117], v[190:191] op_sel:[0,1,0] op_sel_hi:[1,1,1]
	v_pk_mul_f32 v[192:193], v[70:71], v[122:123] op_sel_hi:[1,0]
	v_pk_fma_f32 v[192:193], v[72:73], v[122:123], v[192:193] op_sel:[0,1,0] op_sel_hi:[1,1,1]
	v_pk_fma_f32 v[192:193], v[74:75], v[124:125], v[192:193] op_sel_hi:[1,0,1]
	v_pk_fma_f32 v[192:193], v[76:77], v[124:125], v[192:193] op_sel:[0,1,0] op_sel_hi:[1,1,1]

	s_waitcnt lgkmcnt(0)
	ds_write_b32 v197, v92 offset:3072
	ds_read_b128 v[82:85], v79 offset:0x1e00
	ds_read_b128 v[86:89], v79 offset:0x3e00
	ds_read_b128 v[114:117], v79 offset:0x5e00
	ds_read_b128 v[118:121], v79 offset:0x7e00
	ds_read_b128 v[122:125], v79 offset:0x9e00
	ds_read_b64 v[126:127], v198 offset:7680
	v_pk_mul_f32 v[250:251], v[70:71], v[166:167] op_sel_hi:[1,0]
	v_pk_fma_f32 v[250:251], v[72:73], v[166:167], v[250:251] op_sel:[0,1,0] op_sel_hi:[1,1,1]
	v_pk_fma_f32 v[250:251], v[74:75], v[168:169], v[250:251] op_sel_hi:[1,0,1]
	v_pk_fma_f32 v[250:251], v[76:77], v[168:169], v[250:251] op_sel:[0,1,0] op_sel_hi:[1,1,1]
	v_pk_mul_f32 v[184:185], v[182:183], v[174:175] op_sel_hi:[1,0]
	v_pk_mul_f32 v[186:187], v[182:183], v[174:175] op_sel:[0,1] op_sel_hi:[1,1]
	v_add_f32_dpp v252, v251, v250 quad_perm:[1,0,3,2] row_mask:0xf bank_mask:0xf bound_ctrl:1
	v_add_f32_dpp v161, v193, v192 quad_perm:[1,0,3,2] row_mask:0xf bank_mask:0xf bound_ctrl:1
	v_pk_mul_f32 v[188:189], v[182:183], v[176:177] op_sel_hi:[1,0]
	v_add_f32_dpp v252, v252, v252 quad_perm:[2,3,0,1] row_mask:0xf bank_mask:0xf bound_ctrl:1
	v_add_f32_dpp v161, v161, v161 quad_perm:[2,3,0,1] row_mask:0xf bank_mask:0xf bound_ctrl:1
	v_pk_mul_f32 v[190:191], v[182:183], v[176:177] op_sel:[0,1] op_sel_hi:[1,1]
	v_add_f32_dpp v252, v252, v252 row_ror:4 row_mask:0xf bank_mask:0xf bound_ctrl:1
	v_add_f32_dpp v161, v161, v161 row_ror:4 row_mask:0xf bank_mask:0xf bound_ctrl:1
	v_pk_fma_f32 v[184:185], v[70:71], v[162:163], v[184:185] op_sel_hi:[1,0,1]
	v_add_f32_dpp v252, v252, v252 row_ror:8 row_mask:0xf bank_mask:0xf bound_ctrl:1
	v_add_f32_dpp v92, v161, v161 row_ror:8 row_mask:0xf bank_mask:0x1 bound_ctrl:1
	v_pk_fma_f32 v[186:187], v[72:73], v[162:163], v[186:187] op_sel:[0,1,0] op_sel_hi:[1,1,1]
	v_mov_b32_dpp v253, v252 quad_perm:[1,0,3,2] row_mask:0xf bank_mask:0xf bound_ctrl:1
	v_pk_fma_f32 v[188:189], v[74:75], v[164:165], v[188:189] op_sel_hi:[1,0,1]
	v_pk_fma_f32 v[190:191], v[76:77], v[164:165], v[190:191] op_sel:[0,1,0] op_sel_hi:[1,1,1]
	v_pk_fma_f32 v[70:71], v[252:253], v[170:171], v[184:185] op_sel_hi:[1,0,1]
	v_pk_fma_f32 v[72:73], v[252:253], v[170:171], v[186:187] op_sel:[0,1,0] op_sel_hi:[1,1,1]
	v_pk_fma_f32 v[74:75], v[252:253], v[172:173], v[188:189] op_sel_hi:[1,0,1]
	v_pk_fma_f32 v[76:77], v[252:253], v[172:173], v[190:191] op_sel:[0,1,0] op_sel_hi:[1,1,1]
	v_pk_mul_f32 v[194:195], v[70:71], v[178:179] op_sel_hi:[1,0]
	v_pk_fma_f32 v[194:195], v[72:73], v[178:179], v[194:195] op_sel:[0,1,0] op_sel_hi:[1,1,1]
	v_pk_fma_f32 v[194:195], v[74:75], v[180:181], v[194:195] op_sel_hi:[1,0,1]
	v_pk_fma_f32 v[194:195], v[76:77], v[180:181], v[194:195] op_sel:[0,1,0] op_sel_hi:[1,1,1]

	s_waitcnt lgkmcnt(0)
	ds_read_b128 v[162:165], v79 offset:0x1f00
	ds_read_b128 v[166:169], v79 offset:0x3f00
	ds_read_b128 v[170:173], v79 offset:0x5f00
	ds_read_b128 v[174:177], v79 offset:0x7f00
	ds_read_b128 v[178:181], v79 offset:0x9f00
	ds_read_b64 v[182:183], v198 offset:7936
	v_pk_mul_f32 v[250:251], v[70:71], v[86:87] op_sel_hi:[1,0]
	v_pk_fma_f32 v[250:251], v[72:73], v[86:87], v[250:251] op_sel:[0,1,0] op_sel_hi:[1,1,1]
	v_pk_fma_f32 v[250:251], v[74:75], v[88:89], v[250:251] op_sel_hi:[1,0,1]
	v_pk_fma_f32 v[250:251], v[76:77], v[88:89], v[250:251] op_sel:[0,1,0] op_sel_hi:[1,1,1]
	v_pk_mul_f32 v[184:185], v[126:127], v[118:119] op_sel_hi:[1,0]
	v_pk_mul_f32 v[186:187], v[126:127], v[118:119] op_sel:[0,1] op_sel_hi:[1,1]
	v_add_f32_dpp v252, v251, v250 quad_perm:[1,0,3,2] row_mask:0xf bank_mask:0xf bound_ctrl:1
	v_add_f32_dpp v161, v195, v194 quad_perm:[1,0,3,2] row_mask:0xf bank_mask:0xf bound_ctrl:1
	v_pk_mul_f32 v[188:189], v[126:127], v[120:121] op_sel_hi:[1,0]
	v_add_f32_dpp v252, v252, v252 quad_perm:[2,3,0,1] row_mask:0xf bank_mask:0xf bound_ctrl:1
	v_add_f32_dpp v161, v161, v161 quad_perm:[2,3,0,1] row_mask:0xf bank_mask:0xf bound_ctrl:1
	v_pk_mul_f32 v[190:191], v[126:127], v[120:121] op_sel:[0,1] op_sel_hi:[1,1]
	v_add_f32_dpp v252, v252, v252 row_ror:4 row_mask:0xf bank_mask:0xf bound_ctrl:1
	v_add_f32_dpp v161, v161, v161 row_ror:4 row_mask:0xf bank_mask:0xf bound_ctrl:1
	v_pk_fma_f32 v[184:185], v[70:71], v[82:83], v[184:185] op_sel_hi:[1,0,1]
	v_add_f32_dpp v252, v252, v252 row_ror:8 row_mask:0xf bank_mask:0xf bound_ctrl:1
	v_add_f32_dpp v92, v161, v161 row_ror:8 row_mask:0xf bank_mask:0x2 bound_ctrl:1
	v_pk_fma_f32 v[186:187], v[72:73], v[82:83], v[186:187] op_sel:[0,1,0] op_sel_hi:[1,1,1]
	v_mov_b32_dpp v253, v252 quad_perm:[1,0,3,2] row_mask:0xf bank_mask:0xf bound_ctrl:1
	v_pk_fma_f32 v[188:189], v[74:75], v[84:85], v[188:189] op_sel_hi:[1,0,1]
	v_pk_fma_f32 v[190:191], v[76:77], v[84:85], v[190:191] op_sel:[0,1,0] op_sel_hi:[1,1,1]
	v_pk_fma_f32 v[70:71], v[252:253], v[114:115], v[184:185] op_sel_hi:[1,0,1]
	v_pk_fma_f32 v[72:73], v[252:253], v[114:115], v[186:187] op_sel:[0,1,0] op_sel_hi:[1,1,1]
	v_pk_fma_f32 v[74:75], v[252:253], v[116:117], v[188:189] op_sel_hi:[1,0,1]
	v_pk_fma_f32 v[76:77], v[252:253], v[116:117], v[190:191] op_sel:[0,1,0] op_sel_hi:[1,1,1]
	v_pk_mul_f32 v[192:193], v[70:71], v[122:123] op_sel_hi:[1,0]
	v_pk_fma_f32 v[192:193], v[72:73], v[122:123], v[192:193] op_sel:[0,1,0] op_sel_hi:[1,1,1]
	v_pk_fma_f32 v[192:193], v[74:75], v[124:125], v[192:193] op_sel_hi:[1,0,1]
	v_pk_fma_f32 v[192:193], v[76:77], v[124:125], v[192:193] op_sel:[0,1,0] op_sel_hi:[1,1,1]

	s_waitcnt lgkmcnt(0)
	v_pk_mul_f32 v[250:251], v[70:71], v[166:167] op_sel_hi:[1,0]
	v_pk_fma_f32 v[250:251], v[72:73], v[166:167], v[250:251] op_sel:[0,1,0] op_sel_hi:[1,1,1]
	v_pk_fma_f32 v[250:251], v[74:75], v[168:169], v[250:251] op_sel_hi:[1,0,1]
	v_pk_fma_f32 v[250:251], v[76:77], v[168:169], v[250:251] op_sel:[0,1,0] op_sel_hi:[1,1,1]
	v_pk_mul_f32 v[80:81], v[182:183], v[174:175] op_sel_hi:[1,0]
	v_pk_mul_f32 v[126:127], v[182:183], v[174:175] op_sel:[0,1] op_sel_hi:[1,1]
	v_add_f32_dpp v252, v251, v250 quad_perm:[1,0,3,2] row_mask:0xf bank_mask:0xf bound_ctrl:1
	v_add_f32_dpp v190, v193, v192 quad_perm:[1,0,3,2] row_mask:0xf bank_mask:0xf bound_ctrl:1
	v_pk_mul_f32 v[184:185], v[182:183], v[176:177] op_sel_hi:[1,0]
	v_add_f32_dpp v252, v252, v252 quad_perm:[2,3,0,1] row_mask:0xf bank_mask:0xf bound_ctrl:1
	v_add_f32_dpp v190, v190, v190 quad_perm:[2,3,0,1] row_mask:0xf bank_mask:0xf bound_ctrl:1
	v_pk_mul_f32 v[186:187], v[182:183], v[176:177] op_sel:[0,1] op_sel_hi:[1,1]
	v_add_f32_dpp v252, v252, v252 row_ror:4 row_mask:0xf bank_mask:0xf bound_ctrl:1
	v_add_f32_dpp v190, v190, v190 row_ror:4 row_mask:0xf bank_mask:0xf bound_ctrl:1
	v_pk_fma_f32 v[80:81], v[70:71], v[162:163], v[80:81] op_sel_hi:[1,0,1]
	v_add_f32_dpp v252, v252, v252 row_ror:8 row_mask:0xf bank_mask:0xf bound_ctrl:1
	v_add_f32_dpp v92, v190, v190 row_ror:8 row_mask:0xf bank_mask:0x4 bound_ctrl:1
	v_pk_fma_f32 v[126:127], v[72:73], v[162:163], v[126:127] op_sel:[0,1,0] op_sel_hi:[1,1,1]
	v_mov_b32_dpp v253, v252 quad_perm:[1,0,3,2] row_mask:0xf bank_mask:0xf bound_ctrl:1
	v_pk_fma_f32 v[184:185], v[74:75], v[164:165], v[184:185] op_sel_hi:[1,0,1]
	v_pk_fma_f32 v[186:187], v[76:77], v[164:165], v[186:187] op_sel:[0,1,0] op_sel_hi:[1,1,1]
	v_pk_fma_f32 v[70:71], v[252:253], v[170:171], v[80:81] op_sel_hi:[1,0,1]
	v_pk_fma_f32 v[72:73], v[252:253], v[170:171], v[126:127] op_sel:[0,1,0] op_sel_hi:[1,1,1]
	v_pk_fma_f32 v[74:75], v[252:253], v[172:173], v[184:185] op_sel_hi:[1,0,1]
	v_pk_fma_f32 v[76:77], v[252:253], v[172:173], v[186:187] op_sel:[0,1,0] op_sel_hi:[1,1,1]
	v_pk_mul_f32 v[188:189], v[70:71], v[178:179] op_sel_hi:[1,0]
	v_pk_fma_f32 v[188:189], v[72:73], v[178:179], v[188:189] op_sel:[0,1,0] op_sel_hi:[1,1,1]
	v_pk_fma_f32 v[188:189], v[74:75], v[180:181], v[188:189] op_sel_hi:[1,0,1]
	v_pk_fma_f32 v[188:189], v[76:77], v[180:181], v[188:189] op_sel:[0,1,0] op_sel_hi:[1,1,1]

; __device__ __forceinline__ float pair16_sum(f32x2 p) { float x = p.x + dpp_mov<0xB1>(p.y); x = dpp_add<0x4E>(x); x = dpp_add<0x124>(x); x = dpp_add<0x128>(x); return x; }
; __device__ __forceinline__ void p4_scan(Frame& F) {
;     ...
;                     { const float y7 = pair16_sum(qq); ykeep = ((kap >> 1) == 7) ? y7 : ykeep; }
;                     yb[(24 + (kap >> 1)) * 32 + rown] = ykeep;
;                 }
;     ...
;                 asm volatile("s_waitcnt lgkmcnt(0)" ::: "memory"); __builtin_amdgcn_s_barrier(); asm volatile("" ::: "memory");
	s_waitcnt lgkmcnt(0)
	s_nop 0
	s_nop 0
	v_add_f32_dpp v79, v189, v188 quad_perm:[1,0,3,2] row_mask:0xf bank_mask:0xf bound_ctrl:1
	s_nop 1
	v_add_f32_dpp v79, v79, v79 quad_perm:[2,3,0,1] row_mask:0xf bank_mask:0xf bound_ctrl:1
	s_nop 1
	v_add_f32_dpp v79, v79, v79 row_ror:4 row_mask:0xf bank_mask:0xf bound_ctrl:1
	s_nop 1
	v_add_f32_dpp v92, v79, v79 row_ror:8 row_mask:0xf bank_mask:0x8 bound_ctrl:1
	ds_write_b32 v197, v92 offset:3584
	s_waitcnt lgkmcnt(0)
	s_barrier
	s_cbranch_scc1 .LBB0_489
	s_setprio 0
	s_mov_b64 s[2:3], 0

.LBB0_494:
	s_or_b64 exec, exec, s[2:3]
	s_waitcnt vmcnt(4)
	v_lshlrev_b32_e32 v114, 16, v86
	v_and_b32_e32 v115, 0xffff0000, v86
	v_lshlrev_b32_e32 v116, 16, v87
	v_and_b32_e32 v117, 0xffff0000, v87
	v_lshlrev_b32_e32 v118, 16, v88
	v_and_b32_e32 v119, 0xffff0000, v88
	v_lshlrev_b32_e32 v120, 16, v89
	v_and_b32_e32 v121, 0xffff0000, v89
	v_mul_f32_e32 v86, 0xbfb8aa3b, v114
	v_mul_f32_e32 v87, 0xbfb8aa3b, v115
	v_mul_f32_e32 v88, 0xbfb8aa3b, v116
	v_mul_f32_e32 v89, 0xbfb8aa3b, v117
	v_exp_f32_e32 v86, v86
	v_exp_f32_e32 v87, v87
	v_exp_f32_e32 v88, v88
	v_exp_f32_e32 v89, v89
	v_mul_f32_e32 v114, 0xbfb8aa3b, v118
	v_mul_f32_e32 v115, 0xbfb8aa3b, v119
	v_mul_f32_e32 v116, 0xbfb8aa3b, v120
	v_mul_f32_e32 v117, 0xbfb8aa3b, v121
	v_exp_f32_e32 v114, v114
	v_exp_f32_e32 v115, v115
	v_exp_f32_e32 v116, v116
	v_exp_f32_e32 v117, v117
	ds_write_b128 v137, v[86:89]
	ds_write_b128 v137, v[114:117] offset:16
	s_waitcnt vmcnt(3)
	v_lshlrev_b32_e32 v86, 16, v82
	v_and_b32_e32 v87, 0xffff0000, v82
	v_lshlrev_b32_e32 v88, 16, v83
	v_and_b32_e32 v89, 0xffff0000, v83
	v_lshlrev_b32_e32 v82, 16, v84
	v_and_b32_e32 v83, 0xffff0000, v84
	v_lshlrev_b32_e32 v84, 16, v85
	v_and_b32_e32 v85, 0xffff0000, v85
	ds_write_b128 v137, v[82:85] offset:8208
	s_waitcnt vmcnt(2)
	v_lshlrev_b32_e32 v82, 16, v78
	v_and_b32_e32 v83, 0xffff0000, v78
	v_lshlrev_b32_e32 v84, 16, v79
	v_and_b32_e32 v85, 0xffff0000, v79
	v_lshlrev_b32_e32 v78, 16, v80
	v_and_b32_e32 v79, 0xffff0000, v80
	v_lshlrev_b32_e32 v80, 16, v81
	v_and_b32_e32 v81, 0xffff0000, v81
	ds_write_b128 v137, v[78:81] offset:16400
	s_waitcnt vmcnt(1)
	v_lshlrev_b32_e32 v78, 16, v74
	v_and_b32_e32 v79, 0xffff0000, v74
	v_lshlrev_b32_e32 v80, 16, v75
	v_and_b32_e32 v81, 0xffff0000, v75
	v_lshlrev_b32_e32 v74, 16, v76
	v_and_b32_e32 v75, 0xffff0000, v76
	v_lshlrev_b32_e32 v76, 16, v77
	v_and_b32_e32 v77, 0xffff0000, v77
	ds_write_b128 v137, v[74:77] offset:24592
	s_waitcnt vmcnt(0)
	v_lshlrev_b32_e32 v74, 16, v70
	v_and_b32_e32 v75, 0xffff0000, v70
	v_lshlrev_b32_e32 v76, 16, v71
	v_and_b32_e32 v77, 0xffff0000, v71
	v_lshlrev_b32_e32 v70, 16, v72
	v_and_b32_e32 v71, 0xffff0000, v72
	v_lshlrev_b32_e32 v72, 16, v73
	v_and_b32_e32 v73, 0xffff0000, v73
	ds_write_b128 v137, v[86:89] offset:8192
	ds_write_b128 v137, v[82:85] offset:16384
	ds_write_b128 v137, v[78:81] offset:24576
	ds_write_b128 v137, v[74:77] offset:32768
	ds_write_b128 v137, v[70:73] offset:32784
	s_and_saveexec_b64 s[2:3], s[20:21]
	s_cbranch_execz .LBB0_496
	v_lshlrev_b32_e32 v70, 16, v2
	v_and_b32_e32 v71, 0xffff0000, v2
	v_lshlrev_b32_e32 v72, 16, v3
	v_and_b32_e32 v73, 0xffff0000, v3
	v_add_u32_e32 v199, v132, v131
	v_lshlrev_b32_e32 v199, 1, v199
	v_add_u32_e32 v199, 0x20400, v199
	v_pk_mov_b32 v[200:201], v[70:71], v[70:71] op_sel:[1,0]
	v_pk_mov_b32 v[202:203], v[72:73], v[72:73] op_sel:[1,0]
	ds_write2_b64 v199, v[70:71], v[200:201] offset1:1
	ds_write2_b64 v199, v[72:73], v[202:203] offset0:2 offset1:3
	v_lshlrev_b32_e32 v70, 16, v4
	v_and_b32_e32 v71, 0xffff0000, v4
	v_lshlrev_b32_e32 v72, 16, v5
	v_and_b32_e32 v73, 0xffff0000, v5
	v_pk_mov_b32 v[200:201], v[70:71], v[70:71] op_sel:[1,0]
	v_pk_mov_b32 v[202:203], v[72:73], v[72:73] op_sel:[1,0]
	ds_write2_b64 v199, v[70:71], v[200:201] offset0:4 offset1:5
	ds_write2_b64 v199, v[72:73], v[202:203] offset0:6 offset1:7

.LBB0_505:
	s_waitcnt vmcnt(4)
	v_lshlrev_b32_e32 v114, 16, v86
	v_and_b32_e32 v115, 0xffff0000, v86
	v_lshlrev_b32_e32 v116, 16, v87
	v_and_b32_e32 v117, 0xffff0000, v87
	v_lshlrev_b32_e32 v118, 16, v88
	v_and_b32_e32 v119, 0xffff0000, v88
	v_lshlrev_b32_e32 v120, 16, v89
	v_and_b32_e32 v121, 0xffff0000, v89
	v_mul_f32_e32 v86, 0xbfb8aa3b, v114
	v_mul_f32_e32 v87, 0xbfb8aa3b, v115
	v_mul_f32_e32 v88, 0xbfb8aa3b, v116
	v_mul_f32_e32 v89, 0xbfb8aa3b, v117
	v_exp_f32_e32 v86, v86
	v_exp_f32_e32 v87, v87
	v_exp_f32_e32 v88, v88
	v_exp_f32_e32 v89, v89
	s_waitcnt lgkmcnt(0)
	s_barrier
	ds_write_b128 v137, v[86:89] offset:45056
	v_mul_f32_e32 v86, 0xbfb8aa3b, v118
	v_mul_f32_e32 v87, 0xbfb8aa3b, v119
	v_mul_f32_e32 v88, 0xbfb8aa3b, v120
	v_mul_f32_e32 v89, 0xbfb8aa3b, v121
	v_exp_f32_e32 v86, v86
	v_exp_f32_e32 v87, v87
	v_exp_f32_e32 v88, v88
	v_exp_f32_e32 v89, v89
	ds_write_b128 v137, v[86:89] offset:45072
	s_waitcnt vmcnt(3)
	v_lshlrev_b32_e32 v86, 16, v82
	v_and_b32_e32 v87, 0xffff0000, v82
	v_lshlrev_b32_e32 v88, 16, v83
	v_and_b32_e32 v89, 0xffff0000, v83
	v_lshlrev_b32_e32 v82, 16, v84
	v_and_b32_e32 v83, 0xffff0000, v84
	v_lshlrev_b32_e32 v84, 16, v85
	v_and_b32_e32 v85, 0xffff0000, v85
	ds_write_b128 v137, v[82:85] offset:53264
	s_waitcnt vmcnt(2)
	v_lshlrev_b32_e32 v82, 16, v78
	v_and_b32_e32 v83, 0xffff0000, v78
	v_lshlrev_b32_e32 v84, 16, v79
	v_and_b32_e32 v85, 0xffff0000, v79
	v_lshlrev_b32_e32 v78, 16, v80
	v_and_b32_e32 v79, 0xffff0000, v80
	v_lshlrev_b32_e32 v80, 16, v81
	v_and_b32_e32 v81, 0xffff0000, v81
	ds_write_b128 v137, v[78:81] offset:61456
	s_waitcnt vmcnt(1)
	v_lshlrev_b32_e32 v78, 16, v74
	v_and_b32_e32 v79, 0xffff0000, v74
	v_lshlrev_b32_e32 v80, 16, v75
	v_and_b32_e32 v81, 0xffff0000, v75
	v_lshlrev_b32_e32 v74, 16, v76
	v_and_b32_e32 v75, 0xffff0000, v76
	v_lshlrev_b32_e32 v76, 16, v77
	v_and_b32_e32 v77, 0xffff0000, v77
	ds_write_b128 v138, v[74:77] offset:24592
	s_waitcnt vmcnt(0)
	v_lshlrev_b32_e32 v74, 16, v70
	v_and_b32_e32 v75, 0xffff0000, v70
	v_lshlrev_b32_e32 v76, 16, v71
	v_and_b32_e32 v77, 0xffff0000, v71
	v_lshlrev_b32_e32 v70, 16, v72
	v_and_b32_e32 v71, 0xffff0000, v72
	v_lshlrev_b32_e32 v72, 16, v73
	v_and_b32_e32 v73, 0xffff0000, v73
	ds_write_b128 v137, v[86:89] offset:53248
	ds_write_b128 v137, v[82:85] offset:61440
	ds_write_b128 v138, v[78:81] offset:24576
	ds_write_b128 v138, v[74:77] offset:32768
	ds_write_b128 v138, v[70:73] offset:32784
	s_and_saveexec_b64 s[2:3], s[20:21]
	s_cbranch_execz .LBB0_507
	v_lshlrev_b32_e32 v70, 16, v2
	v_and_b32_e32 v71, 0xffff0000, v2
	v_lshlrev_b32_e32 v72, 16, v3
	v_and_b32_e32 v73, 0xffff0000, v3
	v_add_u32_e32 v199, v132, v131
	v_lshlrev_b32_e32 v199, 1, v199
	v_add_u32_e32 v199, 0x22400, v199
	v_pk_mov_b32 v[200:201], v[70:71], v[70:71] op_sel:[1,0]
	v_pk_mov_b32 v[202:203], v[72:73], v[72:73] op_sel:[1,0]
	ds_write2_b64 v199, v[70:71], v[200:201] offset1:1
	ds_write2_b64 v199, v[72:73], v[202:203] offset0:2 offset1:3
	v_lshlrev_b32_e32 v70, 16, v4
	v_and_b32_e32 v71, 0xffff0000, v4
	v_lshlrev_b32_e32 v72, 16, v5
	v_and_b32_e32 v73, 0xffff0000, v5
	v_pk_mov_b32 v[200:201], v[70:71], v[70:71] op_sel:[1,0]
	v_pk_mov_b32 v[202:203], v[72:73], v[72:73] op_sel:[1,0]
	ds_write2_b64 v199, v[70:71], v[200:201] offset0:4 offset1:5
	ds_write2_b64 v199, v[72:73], v[202:203] offset0:6 offset1:7

.LBB0_520:
	s_waitcnt vmcnt(4)
	v_lshlrev_b32_e32 v126, 16, v86
	v_and_b32_e32 v127, 0xffff0000, v86
	v_lshlrev_b32_e32 v161, 16, v87
	v_and_b32_e32 v162, 0xffff0000, v87
	v_lshlrev_b32_e32 v163, 16, v88
	v_and_b32_e32 v164, 0xffff0000, v88
	v_lshlrev_b32_e32 v165, 16, v89
	v_and_b32_e32 v166, 0xffff0000, v89
	v_mul_f32_e32 v86, 0xbfb8aa3b, v126
	v_mul_f32_e32 v87, 0xbfb8aa3b, v127
	v_mul_f32_e32 v88, 0xbfb8aa3b, v161
	v_mul_f32_e32 v89, 0xbfb8aa3b, v162
	s_bitcmp1_b32 s86, 0
	v_exp_f32_e32 v86, v86
	v_exp_f32_e32 v87, v87
	v_exp_f32_e32 v88, v88
	v_exp_f32_e32 v89, v89
	s_cselect_b32 s2, 0xb000, 0
	s_add_i32 s25, s2, 0
	v_add3_u32 v92, s25, v130, v131
	ds_write_b128 v92, v[86:89]
	v_mul_f32_e32 v86, 0xbfb8aa3b, v163
	v_mul_f32_e32 v87, 0xbfb8aa3b, v164
	v_mul_f32_e32 v88, 0xbfb8aa3b, v165
	v_mul_f32_e32 v89, 0xbfb8aa3b, v166
	v_exp_f32_e32 v86, v86
	v_exp_f32_e32 v87, v87
	v_exp_f32_e32 v88, v88
	v_exp_f32_e32 v89, v89
	ds_write_b128 v92, v[86:89] offset:16
	s_waitcnt vmcnt(3)
	v_lshlrev_b32_e32 v86, 16, v82
	v_and_b32_e32 v87, 0xffff0000, v82
	v_lshlrev_b32_e32 v88, 16, v83
	v_and_b32_e32 v89, 0xffff0000, v83
	v_lshlrev_b32_e32 v82, 16, v84
	v_and_b32_e32 v83, 0xffff0000, v84
	v_lshlrev_b32_e32 v84, 16, v85
	v_and_b32_e32 v85, 0xffff0000, v85
	ds_write_b128 v92, v[82:85] offset:8208
	s_waitcnt vmcnt(2)
	v_lshlrev_b32_e32 v82, 16, v78
	v_and_b32_e32 v83, 0xffff0000, v78
	v_lshlrev_b32_e32 v84, 16, v79
	v_and_b32_e32 v85, 0xffff0000, v79
	v_lshlrev_b32_e32 v78, 16, v80
	v_and_b32_e32 v79, 0xffff0000, v80
	v_lshlrev_b32_e32 v80, 16, v81
	v_and_b32_e32 v81, 0xffff0000, v81
	ds_write_b128 v92, v[78:81] offset:16400
	s_waitcnt vmcnt(1)
	v_lshlrev_b32_e32 v78, 16, v74
	v_and_b32_e32 v79, 0xffff0000, v74
	v_lshlrev_b32_e32 v80, 16, v75
	v_and_b32_e32 v81, 0xffff0000, v75
	v_lshlrev_b32_e32 v74, 16, v76
	v_and_b32_e32 v75, 0xffff0000, v76
	v_lshlrev_b32_e32 v76, 16, v77
	v_and_b32_e32 v77, 0xffff0000, v77
	ds_write_b128 v92, v[74:77] offset:24592
	s_waitcnt vmcnt(0)
	v_lshlrev_b32_e32 v74, 16, v70
	v_and_b32_e32 v75, 0xffff0000, v70
	v_lshlrev_b32_e32 v76, 16, v71
	v_and_b32_e32 v77, 0xffff0000, v71
	v_lshlrev_b32_e32 v70, 16, v72
	v_and_b32_e32 v71, 0xffff0000, v72
	v_lshlrev_b32_e32 v72, 16, v73
	v_and_b32_e32 v73, 0xffff0000, v73
	ds_write_b128 v92, v[86:89] offset:8192
	ds_write_b128 v92, v[82:85] offset:16384
	ds_write_b128 v92, v[78:81] offset:24576
	ds_write_b128 v92, v[74:77] offset:32768
	ds_write_b128 v92, v[70:73] offset:32784
	s_and_saveexec_b64 s[2:3], s[20:21]
	s_cbranch_execz .LBB0_522
	v_add3_u32 v74, s25, v132, v131
	v_lshlrev_b32_e32 v70, 16, v2
	v_and_b32_e32 v71, 0xffff0000, v2
	v_lshlrev_b32_e32 v72, 16, v3
	v_and_b32_e32 v73, 0xffff0000, v3
	v_add_u32_e32 v199, v132, v131
	v_mov_b32_e32 v204, s25
	v_lshrrev_b32_e32 v204, 15, v204
	v_lshlrev_b32_e32 v204, 13, v204
	v_lshl_add_u32 v199, v199, 1, v204
	v_add_u32_e32 v199, 0x20400, v199
	v_pk_mov_b32 v[200:201], v[70:71], v[70:71] op_sel:[1,0]
	v_pk_mov_b32 v[202:203], v[72:73], v[72:73] op_sel:[1,0]
	ds_write2_b64 v199, v[70:71], v[200:201] offset1:1
	ds_write2_b64 v199, v[72:73], v[202:203] offset0:2 offset1:3
	v_lshlrev_b32_e32 v70, 16, v4
	v_and_b32_e32 v71, 0xffff0000, v4
	v_lshlrev_b32_e32 v72, 16, v5
	v_and_b32_e32 v73, 0xffff0000, v5
	v_pk_mov_b32 v[200:201], v[70:71], v[70:71] op_sel:[1,0]
	v_pk_mov_b32 v[202:203], v[72:73], v[72:73] op_sel:[1,0]
	ds_write2_b64 v199, v[70:71], v[200:201] offset0:4 offset1:5
	ds_write2_b64 v199, v[72:73], v[202:203] offset0:6 offset1:7

.LBB0_540:
	s_waitcnt vmcnt(4)
	v_lshlrev_b32_e32 v115, 16, v86
	v_and_b32_e32 v118, 0xffff0000, v86
	v_lshlrev_b32_e32 v119, 16, v87
	v_and_b32_e32 v120, 0xffff0000, v87
	v_lshlrev_b32_e32 v121, 16, v88
	v_and_b32_e32 v122, 0xffff0000, v88
	v_lshlrev_b32_e32 v123, 16, v89
	v_and_b32_e32 v124, 0xffff0000, v89
	v_mul_f32_e32 v86, 0xbfb8aa3b, v115
	v_mul_f32_e32 v87, 0xbfb8aa3b, v118
	v_mul_f32_e32 v88, 0xbfb8aa3b, v119
	v_mul_f32_e32 v89, 0xbfb8aa3b, v120
	v_exp_f32_e32 v86, v86
	v_exp_f32_e32 v87, v87
	v_exp_f32_e32 v88, v88
	v_exp_f32_e32 v89, v89
	s_add_i32 s28, 0, 0xb000
	v_add3_u32 v92, s28, v130, v131
	ds_write_b128 v92, v[86:89]
	v_mul_f32_e32 v86, 0xbfb8aa3b, v121
	v_mul_f32_e32 v87, 0xbfb8aa3b, v122
	v_mul_f32_e32 v88, 0xbfb8aa3b, v123
	v_mul_f32_e32 v89, 0xbfb8aa3b, v124
	v_exp_f32_e32 v86, v86
	v_exp_f32_e32 v87, v87
	v_exp_f32_e32 v88, v88
	v_exp_f32_e32 v89, v89
	ds_write_b128 v92, v[86:89] offset:16
	s_waitcnt vmcnt(3)
	v_lshlrev_b32_e32 v86, 16, v82
	v_and_b32_e32 v87, 0xffff0000, v82
	v_lshlrev_b32_e32 v88, 16, v83
	v_and_b32_e32 v89, 0xffff0000, v83
	v_lshlrev_b32_e32 v82, 16, v84
	v_and_b32_e32 v83, 0xffff0000, v84
	v_lshlrev_b32_e32 v84, 16, v85
	v_and_b32_e32 v85, 0xffff0000, v85
	ds_write_b128 v92, v[82:85] offset:8208
	s_waitcnt vmcnt(2)
	v_lshlrev_b32_e32 v82, 16, v78
	v_and_b32_e32 v83, 0xffff0000, v78
	v_lshlrev_b32_e32 v84, 16, v79
	v_and_b32_e32 v85, 0xffff0000, v79
	v_lshlrev_b32_e32 v78, 16, v80
	v_and_b32_e32 v79, 0xffff0000, v80
	v_lshlrev_b32_e32 v80, 16, v81
	v_and_b32_e32 v81, 0xffff0000, v81
	ds_write_b128 v92, v[78:81] offset:16400
	s_waitcnt vmcnt(1)
	v_lshlrev_b32_e32 v78, 16, v74
	v_and_b32_e32 v79, 0xffff0000, v74
	v_lshlrev_b32_e32 v80, 16, v75
	v_and_b32_e32 v81, 0xffff0000, v75
	v_lshlrev_b32_e32 v74, 16, v76
	v_and_b32_e32 v75, 0xffff0000, v76
	v_lshlrev_b32_e32 v76, 16, v77
	v_and_b32_e32 v77, 0xffff0000, v77
	ds_write_b128 v92, v[74:77] offset:24592
	s_waitcnt vmcnt(0)
	v_lshlrev_b32_e32 v74, 16, v70
	v_and_b32_e32 v75, 0xffff0000, v70
	v_lshlrev_b32_e32 v76, 16, v71
	v_and_b32_e32 v77, 0xffff0000, v71
	v_lshlrev_b32_e32 v70, 16, v72
	v_and_b32_e32 v71, 0xffff0000, v72
	v_lshlrev_b32_e32 v72, 16, v73
	v_and_b32_e32 v73, 0xffff0000, v73
	ds_write_b128 v92, v[86:89] offset:8192
	ds_write_b128 v92, v[82:85] offset:16384
	ds_write_b128 v92, v[78:81] offset:24576
	ds_write_b128 v92, v[74:77] offset:32768
	ds_write_b128 v92, v[70:73] offset:32784
	s_and_saveexec_b64 s[2:3], s[20:21]
	s_cbranch_execz .LBB0_542
	v_add3_u32 v74, s28, v132, v131
	v_lshlrev_b32_e32 v70, 16, v2
	v_and_b32_e32 v71, 0xffff0000, v2
	v_lshlrev_b32_e32 v72, 16, v3
	v_and_b32_e32 v73, 0xffff0000, v3
	v_add_u32_e32 v199, v132, v131
	v_lshlrev_b32_e32 v199, 1, v199
	v_add_u32_e32 v199, 0x22400, v199
	v_pk_mov_b32 v[200:201], v[70:71], v[70:71] op_sel:[1,0]
	v_pk_mov_b32 v[202:203], v[72:73], v[72:73] op_sel:[1,0]
	ds_write2_b64 v199, v[70:71], v[200:201] offset1:1
	ds_write2_b64 v199, v[72:73], v[202:203] offset0:2 offset1:3
	v_lshlrev_b32_e32 v70, 16, v4
	v_and_b32_e32 v71, 0xffff0000, v4
	v_lshlrev_b32_e32 v72, 16, v5
	v_and_b32_e32 v73, 0xffff0000, v5
	v_pk_mov_b32 v[200:201], v[70:71], v[70:71] op_sel:[1,0]
	v_pk_mov_b32 v[202:203], v[72:73], v[72:73] op_sel:[1,0]
	ds_write2_b64 v199, v[70:71], v[200:201] offset0:4 offset1:5
	ds_write2_b64 v199, v[72:73], v[202:203] offset0:6 offset1:7
